# GEMM K loops (dense in-proj/out-proj, down-proj): first pass peeled with zero addend, accumulator clearing removed
# speedup vs baseline: 1.0001x; 1.0001x over previous
.LBB0_254:
	s_add_u32 s28, s84, s22
	s_addc_u32 s29, s85, s23
	s_and_b64 s[36:37], s[44:45], exec
	s_cselect_b32 s35, s29, s39
	s_cselect_b32 s46, s28, s38
	s_add_u32 s36, s86, s26
	s_addc_u32 s37, s87, s27
	s_and_b64 s[44:45], s[44:45], exec
	s_cselect_b32 s47, s37, s43
	s_cselect_b32 s48, s36, s42
	s_add_u32 s38, s38, 0x40080
	s_addc_u32 s39, s39, 0
	s_add_u32 s49, s42, 0x100
	s_addc_u32 s50, s43, 0
	s_mov_b32 s51, -2
	s_add_u32 s42, s38, 0xfffc0080
	s_addc_u32 s43, s39, -1
	s_add_i32 s53, 0, 0x10000
	v_add_u32_e32 v14, s53, v182
	ds_read_b128 v[2:5], v14
	ds_read_b128 v[6:9], v14 offset:1024
	ds_read_b128 v[10:13], v14 offset:2048
	ds_read_b128 v[14:17], v14 offset:3072
	s_cmp_eq_u32 s51, 12
	s_cselect_b32 s45, s35, s43
	s_cselect_b32 s44, s46, s42
	s_cselect_b32 s43, s47, s50
	s_cselect_b32 s42, s48, s49
	v_lshl_add_u64 v[18:19], s[38:39], 0, v[168:169]
	s_add_i32 m0, s14, 0xc000
	ds_read_b128 v[186:189], v184
	ds_read_b128 v[190:193], v184 offset:1024
	ds_read_b128 v[200:203], v184 offset:2048
	ds_read_b128 v[204:207], v184 offset:3072
	ds_read_b128 v[208:211], v184 offset:4096
	ds_read_b128 v[212:215], v184 offset:5120
	ds_read_b128 v[232:235], v184 offset:6144
	ds_read_b128 v[236:239], v184 offset:7168
	global_load_lds_dwordx4 v[18:19], off
	v_lshl_add_u64 v[18:19], s[38:39], 0, v[170:171]
	s_add_i32 m0, s14, 0xe000
	s_nop 0
	global_load_lds_dwordx4 v[18:19], off
	s_waitcnt lgkmcnt(8)
	s_barrier
	s_waitcnt lgkmcnt(0)
	s_setprio 1
	s_waitcnt lgkmcnt(0)
	v_mfma_scale_f32_16x16x128_f8f6f4 v[158:161], v[2:9], v[186:193], 0, v1, v180 op_sel_hi:[0,0,0]
	v_mfma_scale_f32_16x16x128_f8f6f4 v[154:157], v[10:17], v[186:193], 0, v1, v180 op_sel_hi:[0,0,0]
	v_mfma_scale_f32_16x16x128_f8f6f4 v[150:153], v[2:9], v[200:207], 0, v1, v180 op_sel_hi:[0,0,0]
	v_mfma_scale_f32_16x16x128_f8f6f4 v[142:145], v[10:17], v[200:207], 0, v1, v180 op_sel_hi:[0,0,0]
	v_mfma_scale_f32_16x16x128_f8f6f4 v[134:137], v[2:9], v[208:215], 0, v1, v180 op_sel_hi:[0,0,0]
	v_mfma_scale_f32_16x16x128_f8f6f4 v[126:129], v[10:17], v[208:215], 0, v1, v180 op_sel_hi:[0,0,0]
	v_mfma_scale_f32_16x16x128_f8f6f4 v[118:121], v[2:9], v[232:239], 0, v1, v180 op_sel_hi:[0,0,0]
	v_mfma_scale_f32_16x16x128_f8f6f4 v[110:113], v[10:17], v[232:239], 0, v1, v180 op_sel_hi:[0,0,0]
	s_setprio 0
	s_barrier
	s_add_i32 s52, 0, 0x14000
	s_add_i32 s53, s53, s13
	v_add_u32_e32 v30, s52, v182
	v_lshl_add_u64 v[172:173], s[42:43], 0, v[194:195]
	s_mov_b32 m0, s53
	ds_read_b128 v[18:21], v30
	ds_read_b128 v[22:25], v30 offset:1024
	ds_read_b128 v[26:29], v30 offset:2048
	ds_read_b128 v[30:33], v30 offset:3072
	global_load_lds_dwordx4 v[172:173], off
	v_lshl_add_u64 v[174:175], s[42:43], 0, v[166:167]
	s_add_i32 m0, s53, 0x2000
	s_nop 0
	global_load_lds_dwordx4 v[174:175], off
	s_barrier
	s_waitcnt lgkmcnt(0)
	s_setprio 1
	s_waitcnt lgkmcnt(0)
	v_mfma_scale_f32_16x16x128_f8f6f4 v[146:149], v[18:25], v[186:193], 0, v1, v180 op_sel_hi:[0,0,0]
	v_mfma_scale_f32_16x16x128_f8f6f4 v[138:141], v[26:33], v[186:193], 0, v1, v180 op_sel_hi:[0,0,0]
	v_mfma_scale_f32_16x16x128_f8f6f4 v[130:133], v[18:25], v[200:207], 0, v1, v180 op_sel_hi:[0,0,0]
	v_mfma_scale_f32_16x16x128_f8f6f4 v[122:125], v[26:33], v[200:207], 0, v1, v180 op_sel_hi:[0,0,0]
	v_mfma_scale_f32_16x16x128_f8f6f4 v[114:117], v[18:25], v[208:215], 0, v1, v180 op_sel_hi:[0,0,0]
	v_mfma_scale_f32_16x16x128_f8f6f4 v[106:109], v[26:33], v[208:215], 0, v1, v180 op_sel_hi:[0,0,0]
	v_mfma_scale_f32_16x16x128_f8f6f4 v[102:105], v[18:25], v[232:239], 0, v1, v180 op_sel_hi:[0,0,0]
	v_mfma_scale_f32_16x16x128_f8f6f4 v[98:101], v[26:33], v[232:239], 0, v1, v180 op_sel_hi:[0,0,0]
	s_setprio 0
	s_mov_b32 m0, s14
	v_lshl_add_u64 v[176:177], s[44:45], 0, v[162:163]
	s_barrier
	ds_read_b128 v[186:189], v184 offset:16384
	ds_read_b128 v[190:193], v184 offset:17408
	ds_read_b128 v[200:203], v184 offset:18432
	ds_read_b128 v[204:207], v184 offset:19456
	ds_read_b128 v[208:211], v184 offset:20480
	ds_read_b128 v[212:215], v184 offset:21504
	ds_read_b128 v[232:235], v184 offset:22528
	ds_read_b128 v[236:239], v184 offset:23552
	global_load_lds_dwordx4 v[176:177], off
	v_lshl_add_u64 v[178:179], s[44:45], 0, v[164:165]
	s_mov_b32 m0, s16
	s_nop 0
	global_load_lds_dwordx4 v[178:179], off
	s_barrier
	s_waitcnt lgkmcnt(0)
	s_setprio 1
	s_waitcnt lgkmcnt(0)
	v_mfma_scale_f32_16x16x128_f8f6f4 v[94:97], v[2:9], v[186:193], 0, v1, v180 op_sel_hi:[0,0,0]
	v_mfma_scale_f32_16x16x128_f8f6f4 v[90:93], v[10:17], v[186:193], 0, v1, v180 op_sel_hi:[0,0,0]
	v_mfma_scale_f32_16x16x128_f8f6f4 v[86:89], v[2:9], v[200:207], 0, v1, v180 op_sel_hi:[0,0,0]
	v_mfma_scale_f32_16x16x128_f8f6f4 v[78:81], v[10:17], v[200:207], 0, v1, v180 op_sel_hi:[0,0,0]
	v_mfma_scale_f32_16x16x128_f8f6f4 v[70:73], v[2:9], v[208:215], 0, v1, v180 op_sel_hi:[0,0,0]
	v_mfma_scale_f32_16x16x128_f8f6f4 v[62:65], v[10:17], v[208:215], 0, v1, v180 op_sel_hi:[0,0,0]
	v_mfma_scale_f32_16x16x128_f8f6f4 v[54:57], v[2:9], v[232:239], 0, v1, v180 op_sel_hi:[0,0,0]
	v_mfma_scale_f32_16x16x128_f8f6f4 v[46:49], v[10:17], v[232:239], 0, v1, v180 op_sel_hi:[0,0,0]
	s_setprio 0
	s_barrier
	s_add_u32 s54, s42, 0x40000
	s_addc_u32 s55, s43, 0
	s_add_i32 s52, s52, s13
	v_lshl_add_u64 v[2:3], s[54:55], 0, v[194:195]
	s_mov_b32 m0, s52
	s_nop 0
	global_load_lds_dwordx4 v[2:3], off
	v_lshl_add_u64 v[2:3], s[54:55], 0, v[166:167]
	s_add_i32 m0, s52, 0x2000
	s_nop 0
	global_load_lds_dwordx4 v[2:3], off
	s_waitcnt vmcnt(6)
	s_barrier
	s_setprio 1
	v_mfma_scale_f32_16x16x128_f8f6f4 v[82:85], v[18:25], v[186:193], 0, v1, v180 op_sel_hi:[0,0,0]
	v_mfma_scale_f32_16x16x128_f8f6f4 v[74:77], v[26:33], v[186:193], 0, v1, v180 op_sel_hi:[0,0,0]
	v_mfma_scale_f32_16x16x128_f8f6f4 v[66:69], v[18:25], v[200:207], 0, v1, v180 op_sel_hi:[0,0,0]
	v_mfma_scale_f32_16x16x128_f8f6f4 v[58:61], v[26:33], v[200:207], 0, v1, v180 op_sel_hi:[0,0,0]
	v_mfma_scale_f32_16x16x128_f8f6f4 v[50:53], v[18:25], v[208:215], 0, v1, v180 op_sel_hi:[0,0,0]
	v_mfma_scale_f32_16x16x128_f8f6f4 v[42:45], v[26:33], v[208:215], 0, v1, v180 op_sel_hi:[0,0,0]
	v_mfma_scale_f32_16x16x128_f8f6f4 v[38:41], v[18:25], v[232:239], 0, v1, v180 op_sel_hi:[0,0,0]
	v_mfma_scale_f32_16x16x128_f8f6f4 v[34:37], v[26:33], v[232:239], 0, v1, v180 op_sel_hi:[0,0,0]
	s_setprio 0
	s_add_i32 s52, 0, 0x18000
	v_add_u32_e32 v14, s52, v182
	s_barrier
	ds_read_b128 v[2:5], v14
	ds_read_b128 v[6:9], v14 offset:1024
	ds_read_b128 v[10:13], v14 offset:2048
	ds_read_b128 v[14:17], v14 offset:3072
	s_add_u32 s44, s44, 0x40000
	s_addc_u32 s45, s45, 0
	s_mov_b32 m0, s17
	v_lshl_add_u64 v[208:209], s[44:45], 0, v[162:163]
	ds_read_b128 v[18:21], v184 offset:32768
	ds_read_b128 v[22:25], v184 offset:33792
	ds_read_b128 v[26:29], v184 offset:34816
	ds_read_b128 v[30:33], v184 offset:35840
	ds_read_b128 v[186:189], v184 offset:36864
	ds_read_b128 v[190:193], v184 offset:37888
	ds_read_b128 v[200:203], v184 offset:38912
	ds_read_b128 v[204:207], v184 offset:39936
	global_load_lds_dwordx4 v[208:209], off
	v_lshl_add_u64 v[208:209], s[44:45], 0, v[164:165]
	s_mov_b32 m0, s18
	s_nop 0
	global_load_lds_dwordx4 v[208:209], off
	s_waitcnt lgkmcnt(8)
	s_barrier
	s_waitcnt lgkmcnt(0)
	s_setprio 1
	s_waitcnt lgkmcnt(0)
	v_mfma_scale_f32_16x16x128_f8f6f4 v[158:161], v[2:9], v[18:25], v[158:161], v1, v180 op_sel_hi:[0,0,0]
	v_mfma_scale_f32_16x16x128_f8f6f4 v[154:157], v[10:17], v[18:25], v[154:157], v1, v180 op_sel_hi:[0,0,0]
	v_mfma_scale_f32_16x16x128_f8f6f4 v[150:153], v[2:9], v[26:33], v[150:153], v1, v180 op_sel_hi:[0,0,0]
	v_mfma_scale_f32_16x16x128_f8f6f4 v[142:145], v[10:17], v[26:33], v[142:145], v1, v180 op_sel_hi:[0,0,0]
	v_mfma_scale_f32_16x16x128_f8f6f4 v[134:137], v[2:9], v[186:193], v[134:137], v1, v180 op_sel_hi:[0,0,0]
	v_mfma_scale_f32_16x16x128_f8f6f4 v[126:129], v[10:17], v[186:193], v[126:129], v1, v180 op_sel_hi:[0,0,0]
	v_mfma_scale_f32_16x16x128_f8f6f4 v[118:121], v[2:9], v[200:207], v[118:121], v1, v180 op_sel_hi:[0,0,0]
	v_mfma_scale_f32_16x16x128_f8f6f4 v[110:113], v[10:17], v[200:207], v[110:113], v1, v180 op_sel_hi:[0,0,0]
	s_setprio 0
	s_barrier
	s_add_i32 s44, 0, 0x1c000
	s_add_i32 s45, s52, s13
	v_add_u32_e32 v185, s44, v182
	v_lshl_add_u64 v[172:173], v[172:173], 0, s[30:31]
	s_mov_b32 m0, s45
	ds_read_b128 v[208:211], v185
	ds_read_b128 v[212:215], v185 offset:1024
	ds_read_b128 v[232:235], v185 offset:2048
	ds_read_b128 v[236:239], v185 offset:3072
	global_load_lds_dwordx4 v[172:173], off
	v_lshl_add_u64 v[172:173], v[174:175], 0, s[30:31]
	s_add_i32 m0, s45, 0x2000
	s_nop 0
	global_load_lds_dwordx4 v[172:173], off
	s_barrier
	s_waitcnt lgkmcnt(0)
	s_setprio 1
	s_waitcnt lgkmcnt(0)
	v_mfma_scale_f32_16x16x128_f8f6f4 v[146:149], v[208:215], v[18:25], v[146:149], v1, v180 op_sel_hi:[0,0,0]
	v_mfma_scale_f32_16x16x128_f8f6f4 v[138:141], v[232:239], v[18:25], v[138:141], v1, v180 op_sel_hi:[0,0,0]
	v_mfma_scale_f32_16x16x128_f8f6f4 v[130:133], v[208:215], v[26:33], v[130:133], v1, v180 op_sel_hi:[0,0,0]
	v_mfma_scale_f32_16x16x128_f8f6f4 v[122:125], v[232:239], v[26:33], v[122:125], v1, v180 op_sel_hi:[0,0,0]
	v_mfma_scale_f32_16x16x128_f8f6f4 v[114:117], v[208:215], v[186:193], v[114:117], v1, v180 op_sel_hi:[0,0,0]
	v_mfma_scale_f32_16x16x128_f8f6f4 v[106:109], v[232:239], v[186:193], v[106:109], v1, v180 op_sel_hi:[0,0,0]
	v_mfma_scale_f32_16x16x128_f8f6f4 v[102:105], v[208:215], v[200:207], v[102:105], v1, v180 op_sel_hi:[0,0,0]
	v_mfma_scale_f32_16x16x128_f8f6f4 v[98:101], v[232:239], v[200:207], v[98:101], v1, v180 op_sel_hi:[0,0,0]
	s_setprio 0
	s_mov_b32 m0, s2
	v_lshl_add_u64 v[172:173], v[176:177], 0, s[30:31]
	s_barrier
	ds_read_b128 v[18:21], v184 offset:49152
	ds_read_b128 v[22:25], v184 offset:50176
	ds_read_b128 v[26:29], v184 offset:51200
	ds_read_b128 v[30:33], v184 offset:52224
	ds_read_b128 v[186:189], v184 offset:53248
	ds_read_b128 v[190:193], v184 offset:54272
	ds_read_b128 v[200:203], v184 offset:55296
	ds_read_b128 v[204:207], v184 offset:56320
	global_load_lds_dwordx4 v[172:173], off
	v_lshl_add_u64 v[172:173], v[178:179], 0, s[30:31]
	s_mov_b32 m0, s19
	s_nop 0
	global_load_lds_dwordx4 v[172:173], off
	s_barrier
	s_waitcnt lgkmcnt(0)
	s_setprio 1
	s_waitcnt lgkmcnt(0)
	v_mfma_scale_f32_16x16x128_f8f6f4 v[94:97], v[2:9], v[18:25], v[94:97], v1, v180 op_sel_hi:[0,0,0]
	v_mfma_scale_f32_16x16x128_f8f6f4 v[90:93], v[10:17], v[18:25], v[90:93], v1, v180 op_sel_hi:[0,0,0]
	v_mfma_scale_f32_16x16x128_f8f6f4 v[86:89], v[2:9], v[26:33], v[86:89], v1, v180 op_sel_hi:[0,0,0]
	v_mfma_scale_f32_16x16x128_f8f6f4 v[78:81], v[10:17], v[26:33], v[78:81], v1, v180 op_sel_hi:[0,0,0]
	v_mfma_scale_f32_16x16x128_f8f6f4 v[70:73], v[2:9], v[186:193], v[70:73], v1, v180 op_sel_hi:[0,0,0]
	v_mfma_scale_f32_16x16x128_f8f6f4 v[62:65], v[10:17], v[186:193], v[62:65], v1, v180 op_sel_hi:[0,0,0]
	v_mfma_scale_f32_16x16x128_f8f6f4 v[54:57], v[2:9], v[200:207], v[54:57], v1, v180 op_sel_hi:[0,0,0]
	v_mfma_scale_f32_16x16x128_f8f6f4 v[46:49], v[10:17], v[200:207], v[46:49], v1, v180 op_sel_hi:[0,0,0]
	s_setprio 0
	s_barrier
	s_add_u32 s42, s42, 0x40080
	s_addc_u32 s43, s43, 0
	s_add_i32 s44, s44, s13
	v_lshl_add_u64 v[2:3], s[42:43], 0, v[194:195]
	s_mov_b32 m0, s44
	s_nop 0
	global_load_lds_dwordx4 v[2:3], off
	v_lshl_add_u64 v[2:3], s[42:43], 0, v[166:167]
	s_add_i32 m0, s44, 0x2000
	s_nop 0
	global_load_lds_dwordx4 v[2:3], off
	s_waitcnt vmcnt(6)
	s_barrier
	s_setprio 1
	v_mfma_scale_f32_16x16x128_f8f6f4 v[82:85], v[208:215], v[18:25], v[82:85], v1, v180 op_sel_hi:[0,0,0]
	v_mfma_scale_f32_16x16x128_f8f6f4 v[74:77], v[232:239], v[18:25], v[74:77], v1, v180 op_sel_hi:[0,0,0]
	v_mfma_scale_f32_16x16x128_f8f6f4 v[66:69], v[208:215], v[26:33], v[66:69], v1, v180 op_sel_hi:[0,0,0]
	v_mfma_scale_f32_16x16x128_f8f6f4 v[58:61], v[232:239], v[26:33], v[58:61], v1, v180 op_sel_hi:[0,0,0]
	v_mfma_scale_f32_16x16x128_f8f6f4 v[50:53], v[208:215], v[186:193], v[50:53], v1, v180 op_sel_hi:[0,0,0]
	v_mfma_scale_f32_16x16x128_f8f6f4 v[42:45], v[232:239], v[186:193], v[42:45], v1, v180 op_sel_hi:[0,0,0]
	v_mfma_scale_f32_16x16x128_f8f6f4 v[38:41], v[208:215], v[200:207], v[38:41], v1, v180 op_sel_hi:[0,0,0]
	v_mfma_scale_f32_16x16x128_f8f6f4 v[34:37], v[232:239], v[200:207], v[34:37], v1, v180 op_sel_hi:[0,0,0]
	s_setprio 0
	s_add_i32 s51, s51, 2
	s_add_u32 s38, s38, 0x100
	s_addc_u32 s39, s39, 0
	s_add_u32 s49, s49, 0x100
	s_addc_u32 s50, s50, 0
	s_cmp_gt_u32 s51, 13
	s_barrier
	s_cbranch_scc1 .Lpk255_exit

.Lpk255_exit:
	v_add_u32_e32 v4, s25, v183
	v_add_u32_e32 v12, s33, v181
	v_ashrrev_i32_e32 v5, 31, v4
	v_mov_b64_e32 v[2:3], s[4:5]
	v_mad_i64_i32 v[6:7], s[38:39], v12, s20, v[2:3]
	v_lshlrev_b64 v[4:5], 1, v[4:5]
	s_nop 15
	s_nop 15
	v_lshl_add_u64 v[10:11], v[6:7], 0, v[4:5]
	v_cvt_pk_bf16_f32 v6, v158, v159
	v_cvt_pk_bf16_f32 v7, v160, v161
	v_cvt_pk_bf16_f32 v8, v154, v155
	v_cvt_pk_bf16_f32 v9, v156, v157
	global_store_dwordx4 v[10:11], v[6:9], off
	s_and_b64 vcc, exec, s[6:7]
	s_mov_b32 s25, s9
	v_cvt_pk_bf16_f32 v6, v146, v147
	v_cvt_pk_bf16_f32 v7, v148, v149
	v_cvt_pk_bf16_f32 v8, v138, v139
	v_cvt_pk_bf16_f32 v9, v140, v141
	global_store_dwordx4 v[10:11], v[6:9], off offset:256
	s_mov_b32 s33, s8
	s_mov_b64 s[42:43], s[36:37]
	v_add_u32_e32 v6, 16, v12
	v_mad_i64_i32 v[6:7], s[38:39], v6, s20, v[2:3]
	v_lshl_add_u64 v[10:11], v[6:7], 0, v[4:5]
	v_cvt_pk_bf16_f32 v6, v150, v151
	v_cvt_pk_bf16_f32 v7, v152, v153
	v_cvt_pk_bf16_f32 v8, v142, v143
	v_cvt_pk_bf16_f32 v9, v144, v145
	global_store_dwordx4 v[10:11], v[6:9], off
	s_nop 1
	v_cvt_pk_bf16_f32 v6, v130, v131
	v_cvt_pk_bf16_f32 v7, v132, v133
	v_cvt_pk_bf16_f32 v8, v122, v123
	v_cvt_pk_bf16_f32 v9, v124, v125
	global_store_dwordx4 v[10:11], v[6:9], off offset:256
	s_nop 1
	v_add_u32_e32 v6, 32, v12
	v_mad_i64_i32 v[6:7], s[38:39], v6, s20, v[2:3]
	v_lshl_add_u64 v[10:11], v[6:7], 0, v[4:5]
	v_cvt_pk_bf16_f32 v6, v134, v135
	v_cvt_pk_bf16_f32 v7, v136, v137
	v_cvt_pk_bf16_f32 v8, v126, v127
	v_cvt_pk_bf16_f32 v9, v128, v129
	global_store_dwordx4 v[10:11], v[6:9], off
	s_nop 1
	v_cvt_pk_bf16_f32 v6, v114, v115
	v_cvt_pk_bf16_f32 v7, v116, v117
	v_cvt_pk_bf16_f32 v8, v106, v107
	v_cvt_pk_bf16_f32 v9, v108, v109
	global_store_dwordx4 v[10:11], v[6:9], off offset:256
	s_nop 1
	v_add_u32_e32 v6, 48, v12
	v_mad_i64_i32 v[6:7], s[38:39], v6, s20, v[2:3]
	v_lshl_add_u64 v[10:11], v[6:7], 0, v[4:5]
	v_cvt_pk_bf16_f32 v6, v118, v119
	v_cvt_pk_bf16_f32 v7, v120, v121
	v_cvt_pk_bf16_f32 v8, v110, v111
	v_cvt_pk_bf16_f32 v9, v112, v113
	global_store_dwordx4 v[10:11], v[6:9], off
	s_nop 1
	v_cvt_pk_bf16_f32 v6, v102, v103
	v_cvt_pk_bf16_f32 v7, v104, v105
	v_cvt_pk_bf16_f32 v8, v98, v99
	v_cvt_pk_bf16_f32 v9, v100, v101
	global_store_dwordx4 v[10:11], v[6:9], off offset:256
	s_nop 1
	v_add_u32_e32 v6, 0x80, v12
	v_mad_i64_i32 v[6:7], s[38:39], v6, s20, v[2:3]
	v_lshl_add_u64 v[10:11], v[6:7], 0, v[4:5]
	v_cvt_pk_bf16_f32 v6, v94, v95
	v_cvt_pk_bf16_f32 v7, v96, v97
	v_cvt_pk_bf16_f32 v8, v90, v91
	v_cvt_pk_bf16_f32 v9, v92, v93
	global_store_dwordx4 v[10:11], v[6:9], off
	s_nop 1
	v_cvt_pk_bf16_f32 v6, v82, v83
	v_cvt_pk_bf16_f32 v7, v84, v85
	v_cvt_pk_bf16_f32 v8, v74, v75
	v_cvt_pk_bf16_f32 v9, v76, v77
	global_store_dwordx4 v[10:11], v[6:9], off offset:256
	s_nop 1
	v_add_u32_e32 v6, 0x90, v12
	v_mad_i64_i32 v[6:7], s[38:39], v6, s20, v[2:3]
	v_lshl_add_u64 v[10:11], v[6:7], 0, v[4:5]
	v_cvt_pk_bf16_f32 v6, v86, v87
	v_cvt_pk_bf16_f32 v7, v88, v89
	v_cvt_pk_bf16_f32 v8, v78, v79
	v_cvt_pk_bf16_f32 v9, v80, v81
	global_store_dwordx4 v[10:11], v[6:9], off
	s_nop 1
	v_cvt_pk_bf16_f32 v6, v66, v67
	v_cvt_pk_bf16_f32 v7, v68, v69
	v_cvt_pk_bf16_f32 v8, v58, v59
	v_cvt_pk_bf16_f32 v9, v60, v61
	global_store_dwordx4 v[10:11], v[6:9], off offset:256
	s_nop 1
	v_add_u32_e32 v6, 0xa0, v12
	v_mad_i64_i32 v[6:7], s[38:39], v6, s20, v[2:3]
	v_lshl_add_u64 v[10:11], v[6:7], 0, v[4:5]
	v_cvt_pk_bf16_f32 v6, v70, v71
	v_cvt_pk_bf16_f32 v7, v72, v73
	v_cvt_pk_bf16_f32 v8, v62, v63
	v_cvt_pk_bf16_f32 v9, v64, v65
	global_store_dwordx4 v[10:11], v[6:9], off
	s_nop 1
	v_cvt_pk_bf16_f32 v6, v50, v51
	v_cvt_pk_bf16_f32 v7, v52, v53
	v_cvt_pk_bf16_f32 v8, v42, v43
	v_cvt_pk_bf16_f32 v9, v44, v45
	global_store_dwordx4 v[10:11], v[6:9], off offset:256
	s_nop 1
	v_add_u32_e32 v6, 0xb0, v12
	v_mad_i64_i32 v[2:3], s[38:39], v6, s20, v[2:3]
	v_lshl_add_u64 v[6:7], v[2:3], 0, v[4:5]
	v_cvt_pk_bf16_f32 v2, v54, v55
	v_cvt_pk_bf16_f32 v3, v56, v57
	v_cvt_pk_bf16_f32 v4, v46, v47
	v_cvt_pk_bf16_f32 v5, v48, v49
	s_mov_b64 s[38:39], s[28:29]
	global_store_dwordx4 v[6:7], v[2:5], off
	s_nop 1
	v_cvt_pk_bf16_f32 v2, v38, v39
	v_cvt_pk_bf16_f32 v3, v40, v41
	v_cvt_pk_bf16_f32 v4, v34, v35
	v_cvt_pk_bf16_f32 v5, v36, v37
	global_store_dwordx4 v[6:7], v[2:5], off offset:256
	s_cbranch_vccz .LBB0_248
	s_waitcnt vmcnt(0)
	s_cmpk_gt_u32 s10, 0xff
	s_cbranch_scc1 .LBB0_259
	s_barrier

.LBB0_311:
	s_add_u32 s38, s84, s6
	s_addc_u32 s39, s85, s7
	s_and_b64 s[40:41], s[8:9], exec
	s_cselect_b32 s49, s39, s43
	s_cselect_b32 s50, s38, s42
	s_add_u32 s40, s86, s26
	s_addc_u32 s41, s87, s27
	s_and_b64 s[8:9], s[8:9], exec
	s_cselect_b32 s8, s41, s45
	s_cselect_b32 s9, s40, s44
	s_add_u32 s42, s42, 0x80080
	s_addc_u32 s43, s43, 0
	s_add_u32 s51, s44, 0x100
	s_addc_u32 s52, s45, 0
	s_mov_b32 s53, -2
	s_add_u32 s44, s42, 0xfff80080
	s_addc_u32 s45, s43, -1
	s_add_i32 s54, 0, 0x10000
	v_add_u32_e32 v147, s54, v144
	ds_read_b128 v[140:143], v147
	ds_read_b128 v[148:151], v147 offset:1024
	ds_read_b128 v[152:155], v147 offset:2048
	ds_read_b128 v[156:159], v147 offset:3072
	s_cmp_eq_u32 s53, 28
	s_cselect_b32 s47, s49, s45
	s_cselect_b32 s46, s50, s44
	s_cselect_b32 s45, s8, s52
	s_cselect_b32 s44, s9, s51
	v_lshl_add_u64 v[192:193], s[42:43], 0, v[136:137]
	s_add_i32 m0, s14, 0xc000
	ds_read_b128 v[160:163], v146
	ds_read_b128 v[164:167], v146 offset:1024
	ds_read_b128 v[168:171], v146 offset:2048
	ds_read_b128 v[172:175], v146 offset:3072
	ds_read_b128 v[176:179], v146 offset:4096
	ds_read_b128 v[180:183], v146 offset:5120
	ds_read_b128 v[184:187], v146 offset:6144
	ds_read_b128 v[188:191], v146 offset:7168
	global_load_lds_dwordx4 v[192:193], off
	v_lshl_add_u64 v[192:193], s[42:43], 0, v[138:139]
	s_add_i32 m0, s14, 0xe000
	s_nop 0
	global_load_lds_dwordx4 v[192:193], off
	s_waitcnt lgkmcnt(8)
	s_barrier
	s_waitcnt lgkmcnt(0)
	s_setprio 1
	s_waitcnt lgkmcnt(0)
	v_mfma_f32_16x16x32_bf16 v[126:129], v[140:143], v[160:163], 0
	v_mfma_f32_16x16x32_bf16 v[122:125], v[152:155], v[160:163], 0
	v_mfma_f32_16x16x32_bf16 v[118:121], v[140:143], v[168:171], 0
	v_mfma_f32_16x16x32_bf16 v[110:113], v[152:155], v[168:171], 0
	v_mfma_f32_16x16x32_bf16 v[102:105], v[140:143], v[176:179], 0
	v_mfma_f32_16x16x32_bf16 v[94:97], v[152:155], v[176:179], 0
	v_mfma_f32_16x16x32_bf16 v[86:89], v[140:143], v[184:187], 0
	v_mfma_f32_16x16x32_bf16 v[78:81], v[152:155], v[184:187], 0
	v_mfma_f32_16x16x32_bf16 v[126:129], v[148:151], v[164:167], v[126:129]
	v_mfma_f32_16x16x32_bf16 v[122:125], v[156:159], v[164:167], v[122:125]
	v_mfma_f32_16x16x32_bf16 v[118:121], v[148:151], v[172:175], v[118:121]
	v_mfma_f32_16x16x32_bf16 v[110:113], v[156:159], v[172:175], v[110:113]
	v_mfma_f32_16x16x32_bf16 v[102:105], v[148:151], v[180:183], v[102:105]
	v_mfma_f32_16x16x32_bf16 v[94:97], v[156:159], v[180:183], v[94:97]
	v_mfma_f32_16x16x32_bf16 v[86:89], v[148:151], v[188:191], v[86:89]
	v_mfma_f32_16x16x32_bf16 v[78:81], v[156:159], v[188:191], v[78:81]
	s_setprio 0
	s_barrier
	s_add_i32 s56, 0, 0x14000
	s_add_i32 s54, s54, s13
	v_add_u32_e32 v147, s56, v144
	v_lshl_add_u64 v[192:193], s[44:45], 0, v[194:195]
	s_mov_b32 m0, s54
	ds_read_b128 v[200:203], v147
	ds_read_b128 v[204:207], v147 offset:1024
	ds_read_b128 v[208:211], v147 offset:2048
	ds_read_b128 v[212:215], v147 offset:3072
	global_load_lds_dwordx4 v[192:193], off
	v_lshl_add_u64 v[216:217], s[44:45], 0, v[130:131]
	s_add_i32 m0, s54, 0x2000
	s_nop 0
	global_load_lds_dwordx4 v[216:217], off
	s_barrier
	s_waitcnt lgkmcnt(0)
	s_setprio 1
	s_waitcnt lgkmcnt(0)
	v_mfma_f32_16x16x32_bf16 v[114:117], v[200:203], v[160:163], 0
	v_mfma_f32_16x16x32_bf16 v[106:109], v[208:211], v[160:163], 0
	v_mfma_f32_16x16x32_bf16 v[98:101], v[200:203], v[168:171], 0
	v_mfma_f32_16x16x32_bf16 v[90:93], v[208:211], v[168:171], 0
	v_mfma_f32_16x16x32_bf16 v[82:85], v[200:203], v[176:179], 0
	v_mfma_f32_16x16x32_bf16 v[74:77], v[208:211], v[176:179], 0
	v_mfma_f32_16x16x32_bf16 v[70:73], v[200:203], v[184:187], 0
	v_mfma_f32_16x16x32_bf16 v[66:69], v[208:211], v[184:187], 0
	v_mfma_f32_16x16x32_bf16 v[114:117], v[204:207], v[164:167], v[114:117]
	v_mfma_f32_16x16x32_bf16 v[106:109], v[212:215], v[164:167], v[106:109]
	v_mfma_f32_16x16x32_bf16 v[98:101], v[204:207], v[172:175], v[98:101]
	v_mfma_f32_16x16x32_bf16 v[90:93], v[212:215], v[172:175], v[90:93]
	v_mfma_f32_16x16x32_bf16 v[82:85], v[204:207], v[180:183], v[82:85]
	v_mfma_f32_16x16x32_bf16 v[74:77], v[212:215], v[180:183], v[74:77]
	v_mfma_f32_16x16x32_bf16 v[70:73], v[204:207], v[188:191], v[70:73]
	v_mfma_f32_16x16x32_bf16 v[66:69], v[212:215], v[188:191], v[66:69]
	s_setprio 0
	s_mov_b32 m0, s14
	v_lshl_add_u64 v[220:221], s[46:47], 0, v[134:135]
	s_barrier
	ds_read_b128 v[160:163], v146 offset:16384
	ds_read_b128 v[164:167], v146 offset:17408
	ds_read_b128 v[168:171], v146 offset:18432
	ds_read_b128 v[172:175], v146 offset:19456
	ds_read_b128 v[176:179], v146 offset:20480
	ds_read_b128 v[180:183], v146 offset:21504
	ds_read_b128 v[184:187], v146 offset:22528
	ds_read_b128 v[188:191], v146 offset:23552
	global_load_lds_dwordx4 v[220:221], off
	v_lshl_add_u64 v[222:223], s[46:47], 0, v[132:133]
	s_mov_b32 m0, s16
	s_nop 0
	global_load_lds_dwordx4 v[222:223], off
	s_barrier
	s_waitcnt lgkmcnt(0)
	s_setprio 1
	s_waitcnt lgkmcnt(0)
	v_mfma_f32_16x16x32_bf16 v[62:65], v[140:143], v[160:163], 0
	v_mfma_f32_16x16x32_bf16 v[58:61], v[152:155], v[160:163], 0
	v_mfma_f32_16x16x32_bf16 v[54:57], v[140:143], v[168:171], 0
	v_mfma_f32_16x16x32_bf16 v[46:49], v[152:155], v[168:171], 0
	v_mfma_f32_16x16x32_bf16 v[38:41], v[140:143], v[176:179], 0
	v_mfma_f32_16x16x32_bf16 v[30:33], v[152:155], v[176:179], 0
	v_mfma_f32_16x16x32_bf16 v[22:25], v[140:143], v[184:187], 0
	v_mfma_f32_16x16x32_bf16 v[14:17], v[152:155], v[184:187], 0
	v_mfma_f32_16x16x32_bf16 v[62:65], v[148:151], v[164:167], v[62:65]
	v_mfma_f32_16x16x32_bf16 v[58:61], v[156:159], v[164:167], v[58:61]
	v_mfma_f32_16x16x32_bf16 v[54:57], v[148:151], v[172:175], v[54:57]
	v_mfma_f32_16x16x32_bf16 v[46:49], v[156:159], v[172:175], v[46:49]
	v_mfma_f32_16x16x32_bf16 v[38:41], v[148:151], v[180:183], v[38:41]
	v_mfma_f32_16x16x32_bf16 v[30:33], v[156:159], v[180:183], v[30:33]
	v_mfma_f32_16x16x32_bf16 v[22:25], v[148:151], v[188:191], v[22:25]
	v_mfma_f32_16x16x32_bf16 v[14:17], v[156:159], v[188:191], v[14:17]
	s_setprio 0
	s_barrier
	s_add_u32 s54, s44, 0x80000
	s_addc_u32 s55, s45, 0
	s_add_i32 s56, s56, s13
	v_lshl_add_u64 v[140:141], s[54:55], 0, v[194:195]
	s_mov_b32 m0, s56
	s_nop 0
	global_load_lds_dwordx4 v[140:141], off
	v_lshl_add_u64 v[140:141], s[54:55], 0, v[130:131]
	s_add_i32 m0, s56, 0x2000
	s_nop 0
	global_load_lds_dwordx4 v[140:141], off
	s_waitcnt vmcnt(6)
	s_barrier
	s_setprio 1
	v_mfma_f32_16x16x32_bf16 v[50:53], v[200:203], v[160:163], 0
	v_mfma_f32_16x16x32_bf16 v[42:45], v[208:211], v[160:163], 0
	v_mfma_f32_16x16x32_bf16 v[34:37], v[200:203], v[168:171], 0
	v_mfma_f32_16x16x32_bf16 v[26:29], v[208:211], v[168:171], 0
	v_mfma_f32_16x16x32_bf16 v[18:21], v[200:203], v[176:179], 0
	v_mfma_f32_16x16x32_bf16 v[10:13], v[208:211], v[176:179], 0
	v_mfma_f32_16x16x32_bf16 v[6:9], v[200:203], v[184:187], 0
	v_mfma_f32_16x16x32_bf16 v[2:5], v[208:211], v[184:187], 0
	v_mfma_f32_16x16x32_bf16 v[50:53], v[204:207], v[164:167], v[50:53]
	v_mfma_f32_16x16x32_bf16 v[42:45], v[212:215], v[164:167], v[42:45]
	v_mfma_f32_16x16x32_bf16 v[34:37], v[204:207], v[172:175], v[34:37]
	v_mfma_f32_16x16x32_bf16 v[26:29], v[212:215], v[172:175], v[26:29]
	v_mfma_f32_16x16x32_bf16 v[18:21], v[204:207], v[180:183], v[18:21]
	v_mfma_f32_16x16x32_bf16 v[10:13], v[212:215], v[180:183], v[10:13]
	v_mfma_f32_16x16x32_bf16 v[6:9], v[204:207], v[188:191], v[6:9]
	v_mfma_f32_16x16x32_bf16 v[2:5], v[212:215], v[188:191], v[2:5]
	s_setprio 0
	s_add_i32 s54, 0, 0x18000
	v_add_u32_e32 v147, s54, v144
	s_barrier
	ds_read_b128 v[140:143], v147
	ds_read_b128 v[148:151], v147 offset:1024
	ds_read_b128 v[152:155], v147 offset:2048
	ds_read_b128 v[156:159], v147 offset:3072
	s_add_u32 s46, s46, 0x80000
	s_addc_u32 s47, s47, 0
	s_mov_b32 m0, s17
	v_lshl_add_u64 v[200:201], s[46:47], 0, v[134:135]
	ds_read_b128 v[160:163], v146 offset:32768
	ds_read_b128 v[164:167], v146 offset:33792
	ds_read_b128 v[168:171], v146 offset:34816
	ds_read_b128 v[172:175], v146 offset:35840
	ds_read_b128 v[176:179], v146 offset:36864
	ds_read_b128 v[180:183], v146 offset:37888
	ds_read_b128 v[184:187], v146 offset:38912
	ds_read_b128 v[188:191], v146 offset:39936
	global_load_lds_dwordx4 v[200:201], off
	v_lshl_add_u64 v[200:201], s[46:47], 0, v[132:133]
	s_mov_b32 m0, s18
	s_nop 0
	global_load_lds_dwordx4 v[200:201], off
	s_waitcnt lgkmcnt(8)
	s_barrier
	s_waitcnt lgkmcnt(0)
	s_setprio 1
	s_waitcnt lgkmcnt(0)
	v_mfma_f32_16x16x32_bf16 v[126:129], v[140:143], v[160:163], v[126:129]
	v_mfma_f32_16x16x32_bf16 v[122:125], v[152:155], v[160:163], v[122:125]
	v_mfma_f32_16x16x32_bf16 v[118:121], v[140:143], v[168:171], v[118:121]
	v_mfma_f32_16x16x32_bf16 v[110:113], v[152:155], v[168:171], v[110:113]
	v_mfma_f32_16x16x32_bf16 v[102:105], v[140:143], v[176:179], v[102:105]
	v_mfma_f32_16x16x32_bf16 v[94:97], v[152:155], v[176:179], v[94:97]
	v_mfma_f32_16x16x32_bf16 v[86:89], v[140:143], v[184:187], v[86:89]
	v_mfma_f32_16x16x32_bf16 v[78:81], v[152:155], v[184:187], v[78:81]
	v_mfma_f32_16x16x32_bf16 v[126:129], v[148:151], v[164:167], v[126:129]
	v_mfma_f32_16x16x32_bf16 v[122:125], v[156:159], v[164:167], v[122:125]
	v_mfma_f32_16x16x32_bf16 v[118:121], v[148:151], v[172:175], v[118:121]
	v_mfma_f32_16x16x32_bf16 v[110:113], v[156:159], v[172:175], v[110:113]
	v_mfma_f32_16x16x32_bf16 v[102:105], v[148:151], v[180:183], v[102:105]
	v_mfma_f32_16x16x32_bf16 v[94:97], v[156:159], v[180:183], v[94:97]
	v_mfma_f32_16x16x32_bf16 v[86:89], v[148:151], v[188:191], v[86:89]
	v_mfma_f32_16x16x32_bf16 v[78:81], v[156:159], v[188:191], v[78:81]
	s_setprio 0
	s_barrier
	s_add_i32 s46, 0, 0x1c000
	s_add_i32 s47, s54, s13
	v_add_u32_e32 v147, s46, v144
	v_lshl_add_u64 v[192:193], v[192:193], 0, s[30:31]
	s_mov_b32 m0, s47
	ds_read_b128 v[200:203], v147
	ds_read_b128 v[204:207], v147 offset:1024
	ds_read_b128 v[208:211], v147 offset:2048
	ds_read_b128 v[212:215], v147 offset:3072
	global_load_lds_dwordx4 v[192:193], off
	v_lshl_add_u64 v[192:193], v[216:217], 0, s[30:31]
	s_add_i32 m0, s47, 0x2000
	s_nop 0
	global_load_lds_dwordx4 v[192:193], off
	s_barrier
	s_waitcnt lgkmcnt(0)
	s_setprio 1
	s_waitcnt lgkmcnt(0)
	v_mfma_f32_16x16x32_bf16 v[114:117], v[200:203], v[160:163], v[114:117]
	v_mfma_f32_16x16x32_bf16 v[106:109], v[208:211], v[160:163], v[106:109]
	v_mfma_f32_16x16x32_bf16 v[98:101], v[200:203], v[168:171], v[98:101]
	v_mfma_f32_16x16x32_bf16 v[90:93], v[208:211], v[168:171], v[90:93]
	v_mfma_f32_16x16x32_bf16 v[82:85], v[200:203], v[176:179], v[82:85]
	v_mfma_f32_16x16x32_bf16 v[74:77], v[208:211], v[176:179], v[74:77]
	v_mfma_f32_16x16x32_bf16 v[70:73], v[200:203], v[184:187], v[70:73]
	v_mfma_f32_16x16x32_bf16 v[66:69], v[208:211], v[184:187], v[66:69]
	v_mfma_f32_16x16x32_bf16 v[114:117], v[204:207], v[164:167], v[114:117]
	v_mfma_f32_16x16x32_bf16 v[106:109], v[212:215], v[164:167], v[106:109]
	v_mfma_f32_16x16x32_bf16 v[98:101], v[204:207], v[172:175], v[98:101]
	v_mfma_f32_16x16x32_bf16 v[90:93], v[212:215], v[172:175], v[90:93]
	v_mfma_f32_16x16x32_bf16 v[82:85], v[204:207], v[180:183], v[82:85]
	v_mfma_f32_16x16x32_bf16 v[74:77], v[212:215], v[180:183], v[74:77]
	v_mfma_f32_16x16x32_bf16 v[70:73], v[204:207], v[188:191], v[70:73]
	v_mfma_f32_16x16x32_bf16 v[66:69], v[212:215], v[188:191], v[66:69]
	s_setprio 0
	s_mov_b32 m0, s2
	v_lshl_add_u64 v[192:193], v[220:221], 0, s[30:31]
	s_barrier
	ds_read_b128 v[160:163], v146 offset:49152
	ds_read_b128 v[164:167], v146 offset:50176
	ds_read_b128 v[168:171], v146 offset:51200
	ds_read_b128 v[172:175], v146 offset:52224
	ds_read_b128 v[176:179], v146 offset:53248
	ds_read_b128 v[180:183], v146 offset:54272
	ds_read_b128 v[184:187], v146 offset:55296
	ds_read_b128 v[188:191], v146 offset:56320
	global_load_lds_dwordx4 v[192:193], off
	v_lshl_add_u64 v[192:193], v[222:223], 0, s[30:31]
	s_mov_b32 m0, s19
	s_nop 0
	global_load_lds_dwordx4 v[192:193], off
	s_barrier
	s_waitcnt lgkmcnt(0)
	s_setprio 1
	s_waitcnt lgkmcnt(0)
	v_mfma_f32_16x16x32_bf16 v[62:65], v[140:143], v[160:163], v[62:65]
	v_mfma_f32_16x16x32_bf16 v[58:61], v[152:155], v[160:163], v[58:61]
	v_mfma_f32_16x16x32_bf16 v[54:57], v[140:143], v[168:171], v[54:57]
	v_mfma_f32_16x16x32_bf16 v[46:49], v[152:155], v[168:171], v[46:49]
	v_mfma_f32_16x16x32_bf16 v[38:41], v[140:143], v[176:179], v[38:41]
	v_mfma_f32_16x16x32_bf16 v[30:33], v[152:155], v[176:179], v[30:33]
	v_mfma_f32_16x16x32_bf16 v[22:25], v[140:143], v[184:187], v[22:25]
	v_mfma_f32_16x16x32_bf16 v[14:17], v[152:155], v[184:187], v[14:17]
	v_mfma_f32_16x16x32_bf16 v[62:65], v[148:151], v[164:167], v[62:65]
	v_mfma_f32_16x16x32_bf16 v[58:61], v[156:159], v[164:167], v[58:61]
	v_mfma_f32_16x16x32_bf16 v[54:57], v[148:151], v[172:175], v[54:57]
	v_mfma_f32_16x16x32_bf16 v[46:49], v[156:159], v[172:175], v[46:49]
	v_mfma_f32_16x16x32_bf16 v[38:41], v[148:151], v[180:183], v[38:41]
	v_mfma_f32_16x16x32_bf16 v[30:33], v[156:159], v[180:183], v[30:33]
	v_mfma_f32_16x16x32_bf16 v[22:25], v[148:151], v[188:191], v[22:25]
	v_mfma_f32_16x16x32_bf16 v[14:17], v[156:159], v[188:191], v[14:17]
	s_setprio 0
	s_barrier
	s_add_u32 s44, s44, 0x80080
	s_addc_u32 s45, s45, 0
	s_add_i32 s46, s46, s13
	v_lshl_add_u64 v[140:141], s[44:45], 0, v[194:195]
	s_mov_b32 m0, s46
	s_nop 0
	global_load_lds_dwordx4 v[140:141], off
	v_lshl_add_u64 v[140:141], s[44:45], 0, v[130:131]
	s_add_i32 m0, s46, 0x2000
	s_nop 0
	global_load_lds_dwordx4 v[140:141], off
	s_waitcnt vmcnt(6)
	s_barrier
	s_setprio 1
	v_mfma_f32_16x16x32_bf16 v[50:53], v[200:203], v[160:163], v[50:53]
	v_mfma_f32_16x16x32_bf16 v[42:45], v[208:211], v[160:163], v[42:45]
	v_mfma_f32_16x16x32_bf16 v[34:37], v[200:203], v[168:171], v[34:37]
	v_mfma_f32_16x16x32_bf16 v[26:29], v[208:211], v[168:171], v[26:29]
	v_mfma_f32_16x16x32_bf16 v[18:21], v[200:203], v[176:179], v[18:21]
	v_mfma_f32_16x16x32_bf16 v[10:13], v[208:211], v[176:179], v[10:13]
	v_mfma_f32_16x16x32_bf16 v[6:9], v[200:203], v[184:187], v[6:9]
	v_mfma_f32_16x16x32_bf16 v[2:5], v[208:211], v[184:187], v[2:5]
	v_mfma_f32_16x16x32_bf16 v[50:53], v[204:207], v[164:167], v[50:53]
	v_mfma_f32_16x16x32_bf16 v[42:45], v[212:215], v[164:167], v[42:45]
	v_mfma_f32_16x16x32_bf16 v[34:37], v[204:207], v[172:175], v[34:37]
	v_mfma_f32_16x16x32_bf16 v[26:29], v[212:215], v[172:175], v[26:29]
	v_mfma_f32_16x16x32_bf16 v[18:21], v[204:207], v[180:183], v[18:21]
	v_mfma_f32_16x16x32_bf16 v[10:13], v[212:215], v[180:183], v[10:13]
	v_mfma_f32_16x16x32_bf16 v[6:9], v[204:207], v[188:191], v[6:9]
	v_mfma_f32_16x16x32_bf16 v[2:5], v[212:215], v[188:191], v[2:5]
	s_setprio 0
	s_add_i32 s53, s53, 2
	s_add_u32 s42, s42, 0x100
	s_addc_u32 s43, s43, 0
	s_add_u32 s51, s51, 0x100
	s_addc_u32 s52, s52, 0
	s_cmp_gt_u32 s53, 29
	s_barrier
	s_cbranch_scc1 .Lpk312_exit

.Lpk312_exit:
	v_add_u32_e32 v142, s35, v145
	v_add_u32_e32 v147, s48, v1
	v_ashrrev_i32_e32 v143, 31, v142
	v_mov_b64_e32 v[140:141], s[4:5]
	v_mad_i64_i32 v[148:149], s[8:9], v147, s20, v[140:141]
	v_lshlrev_b64 v[142:143], 1, v[142:143]
	v_lshl_add_u64 v[148:149], v[148:149], 0, v[142:143]
	v_cvt_pk_bf16_f32 v126, v126, v127
	v_cvt_pk_bf16_f32 v127, v128, v129
	v_cvt_pk_bf16_f32 v128, v122, v123
	v_cvt_pk_bf16_f32 v129, v124, v125
	global_store_dwordx4 v[148:149], v[126:129], off
	v_cvt_pk_bf16_f32 v114, v114, v115
	v_cvt_pk_bf16_f32 v115, v116, v117
	v_cvt_pk_bf16_f32 v116, v106, v107
	v_add_u32_e32 v106, 16, v147
	v_mad_i64_i32 v[106:107], s[8:9], v106, s20, v[140:141]
	v_cvt_pk_bf16_f32 v117, v108, v109
	global_store_dwordx4 v[148:149], v[114:117], off offset:256
	s_and_b64 vcc, exec, s[36:37]
	s_mov_b32 s35, s25
	v_lshl_add_u64 v[114:115], v[106:107], 0, v[142:143]
	v_cvt_pk_bf16_f32 v106, v118, v119
	v_cvt_pk_bf16_f32 v107, v120, v121
	v_cvt_pk_bf16_f32 v108, v110, v111
	v_cvt_pk_bf16_f32 v109, v112, v113
	global_store_dwordx4 v[114:115], v[106:109], off
	v_cvt_pk_bf16_f32 v98, v98, v99
	v_cvt_pk_bf16_f32 v99, v100, v101
	v_cvt_pk_bf16_f32 v100, v90, v91
	v_add_u32_e32 v90, 32, v147
	v_mad_i64_i32 v[90:91], s[8:9], v90, s20, v[140:141]
	v_cvt_pk_bf16_f32 v101, v92, v93
	global_store_dwordx4 v[114:115], v[98:101], off offset:256
	s_mov_b32 s48, s33
	s_mov_b64 s[44:45], s[40:41]
	v_lshl_add_u64 v[98:99], v[90:91], 0, v[142:143]
	v_cvt_pk_bf16_f32 v90, v102, v103
	v_cvt_pk_bf16_f32 v91, v104, v105
	v_cvt_pk_bf16_f32 v92, v94, v95
	v_cvt_pk_bf16_f32 v93, v96, v97
	global_store_dwordx4 v[98:99], v[90:93], off
	v_cvt_pk_bf16_f32 v82, v82, v83
	v_cvt_pk_bf16_f32 v83, v84, v85
	v_cvt_pk_bf16_f32 v84, v74, v75
	v_add_u32_e32 v74, 48, v147
	v_mad_i64_i32 v[74:75], s[8:9], v74, s20, v[140:141]
	v_cvt_pk_bf16_f32 v85, v76, v77
	global_store_dwordx4 v[98:99], v[82:85], off offset:256
	s_mov_b64 s[42:43], s[38:39]
	s_nop 0
	v_lshl_add_u64 v[82:83], v[74:75], 0, v[142:143]
	v_cvt_pk_bf16_f32 v74, v86, v87
	v_cvt_pk_bf16_f32 v75, v88, v89
	v_cvt_pk_bf16_f32 v76, v78, v79
	v_cvt_pk_bf16_f32 v77, v80, v81
	global_store_dwordx4 v[82:83], v[74:77], off
	v_cvt_pk_bf16_f32 v70, v70, v71
	v_cvt_pk_bf16_f32 v71, v72, v73
	v_cvt_pk_bf16_f32 v72, v66, v67
	v_add_u32_e32 v66, 0x80, v147
	v_mad_i64_i32 v[66:67], s[8:9], v66, s20, v[140:141]
	v_lshl_add_u64 v[66:67], v[66:67], 0, v[142:143]
	v_cvt_pk_bf16_f32 v73, v68, v69
	global_store_dwordx4 v[82:83], v[70:73], off offset:256
	v_cvt_pk_bf16_f32 v62, v62, v63
	v_cvt_pk_bf16_f32 v63, v64, v65
	v_cvt_pk_bf16_f32 v64, v58, v59
	v_cvt_pk_bf16_f32 v65, v60, v61
	global_store_dwordx4 v[66:67], v[62:65], off
	v_cvt_pk_bf16_f32 v50, v50, v51
	v_cvt_pk_bf16_f32 v51, v52, v53
	v_cvt_pk_bf16_f32 v52, v42, v43
	v_add_u32_e32 v42, 0x90, v147
	v_mad_i64_i32 v[42:43], s[8:9], v42, s20, v[140:141]
	v_cvt_pk_bf16_f32 v53, v44, v45
	global_store_dwordx4 v[66:67], v[50:53], off offset:256
	s_nop 1
	v_lshl_add_u64 v[50:51], v[42:43], 0, v[142:143]
	v_cvt_pk_bf16_f32 v42, v54, v55
	v_cvt_pk_bf16_f32 v43, v56, v57
	v_cvt_pk_bf16_f32 v44, v46, v47
	v_cvt_pk_bf16_f32 v45, v48, v49
	global_store_dwordx4 v[50:51], v[42:45], off
	v_cvt_pk_bf16_f32 v34, v34, v35
	v_cvt_pk_bf16_f32 v35, v36, v37
	v_cvt_pk_bf16_f32 v36, v26, v27
	v_add_u32_e32 v26, 0xa0, v147
	v_mad_i64_i32 v[26:27], s[8:9], v26, s20, v[140:141]
	v_cvt_pk_bf16_f32 v37, v28, v29
	global_store_dwordx4 v[50:51], v[34:37], off offset:256
	s_nop 1
	v_lshl_add_u64 v[34:35], v[26:27], 0, v[142:143]
	v_cvt_pk_bf16_f32 v26, v38, v39
	v_cvt_pk_bf16_f32 v27, v40, v41
	v_cvt_pk_bf16_f32 v28, v30, v31
	v_cvt_pk_bf16_f32 v29, v32, v33
	global_store_dwordx4 v[34:35], v[26:29], off
	v_cvt_pk_bf16_f32 v18, v18, v19
	v_cvt_pk_bf16_f32 v19, v20, v21
	v_cvt_pk_bf16_f32 v20, v10, v11
	v_add_u32_e32 v10, 0xb0, v147
	v_mad_i64_i32 v[10:11], s[8:9], v10, s20, v[140:141]
	v_cvt_pk_bf16_f32 v21, v12, v13
	global_store_dwordx4 v[34:35], v[18:21], off offset:256
	s_nop 1
	v_lshl_add_u64 v[18:19], v[10:11], 0, v[142:143]
	v_cvt_pk_bf16_f32 v10, v22, v23
	v_cvt_pk_bf16_f32 v11, v24, v25
	v_cvt_pk_bf16_f32 v12, v14, v15
	v_cvt_pk_bf16_f32 v13, v16, v17
	global_store_dwordx4 v[18:19], v[10:13], off
	v_cvt_pk_bf16_f32 v6, v6, v7
	v_cvt_pk_bf16_f32 v7, v8, v9
	v_cvt_pk_bf16_f32 v8, v2, v3
	v_cvt_pk_bf16_f32 v9, v4, v5
	global_store_dwordx4 v[18:19], v[6:9], off offset:256
	s_cbranch_vccz .LBB0_309
	s_waitcnt vmcnt(0)
	s_cmpk_gt_u32 s10, 0xff
	s_cbranch_scc1 .LBB0_316
	s_barrier

.LBB0_682:
	s_add_u32 s28, s2, s22
	s_addc_u32 s29, s44, s23
	s_and_b64 s[36:37], s[42:43], exec
	s_cselect_b32 s47, s29, s39
	s_cselect_b32 s48, s28, s38
	s_add_u32 s36, s45, s26
	s_addc_u32 s37, s46, s27
	s_and_b64 s[42:43], s[42:43], exec
	s_cselect_b32 s49, s37, s41
	s_cselect_b32 s50, s36, s40
	s_add_u32 s38, s38, 0x80080
	s_addc_u32 s39, s39, 0
	s_add_u32 s51, s40, 0x100
	s_addc_u32 s52, s41, 0
	s_mov_b32 s53, -2
	s_add_u32 s40, s38, 0xfff80080
	s_addc_u32 s41, s39, -1
	s_add_i32 s54, 0, 0x10000
	v_add_u32_e32 v140, s54, v142
	ds_read_b128 v[146:149], v140
	ds_read_b128 v[150:153], v140 offset:1024
	ds_read_b128 v[154:157], v140 offset:2048
	ds_read_b128 v[158:161], v140 offset:3072
	s_cmp_eq_u32 s53, 28
	s_cselect_b32 s43, s47, s41
	s_cselect_b32 s42, s48, s40
	s_cselect_b32 s41, s49, s52
	s_cselect_b32 s40, s50, s51
	v_lshl_add_u64 v[140:141], s[38:39], 0, v[136:137]
	s_add_i32 m0, s14, 0xc000
	ds_read_b128 v[162:165], v144
	ds_read_b128 v[166:169], v144 offset:1024
	ds_read_b128 v[170:173], v144 offset:2048
	ds_read_b128 v[174:177], v144 offset:3072
	ds_read_b128 v[178:181], v144 offset:4096
	ds_read_b128 v[182:185], v144 offset:5120
	ds_read_b128 v[186:189], v144 offset:6144
	ds_read_b128 v[190:193], v144 offset:7168
	global_load_lds_dwordx4 v[140:141], off
	v_lshl_add_u64 v[140:141], s[38:39], 0, v[138:139]
	s_add_i32 m0, s14, 0xe000
	s_nop 0
	global_load_lds_dwordx4 v[140:141], off
	s_waitcnt lgkmcnt(8)
	s_barrier
	s_waitcnt lgkmcnt(0)
	s_setprio 1
	s_waitcnt lgkmcnt(0)
	v_mfma_f32_16x16x32_bf16 v[126:129], v[146:149], v[162:165], 0
	v_mfma_f32_16x16x32_bf16 v[122:125], v[154:157], v[162:165], 0
	v_mfma_f32_16x16x32_bf16 v[118:121], v[146:149], v[170:173], 0
	v_mfma_f32_16x16x32_bf16 v[110:113], v[154:157], v[170:173], 0
	v_mfma_f32_16x16x32_bf16 v[102:105], v[146:149], v[178:181], 0
	v_mfma_f32_16x16x32_bf16 v[94:97], v[154:157], v[178:181], 0
	v_mfma_f32_16x16x32_bf16 v[86:89], v[146:149], v[186:189], 0
	v_mfma_f32_16x16x32_bf16 v[78:81], v[154:157], v[186:189], 0
	v_mfma_f32_16x16x32_bf16 v[126:129], v[150:153], v[166:169], v[126:129]
	v_mfma_f32_16x16x32_bf16 v[122:125], v[158:161], v[166:169], v[122:125]
	v_mfma_f32_16x16x32_bf16 v[118:121], v[150:153], v[174:177], v[118:121]
	v_mfma_f32_16x16x32_bf16 v[110:113], v[158:161], v[174:177], v[110:113]
	v_mfma_f32_16x16x32_bf16 v[102:105], v[150:153], v[182:185], v[102:105]
	v_mfma_f32_16x16x32_bf16 v[94:97], v[158:161], v[182:185], v[94:97]
	v_mfma_f32_16x16x32_bf16 v[86:89], v[150:153], v[190:193], v[86:89]
	v_mfma_f32_16x16x32_bf16 v[78:81], v[158:161], v[190:193], v[78:81]
	s_setprio 0
	s_barrier
	s_add_i32 s56, 0, 0x14000
	v_add_u32_e32 v140, s56, v142
	s_add_i32 s54, s54, s13
	ds_read_b128 v[200:203], v140
	ds_read_b128 v[204:207], v140 offset:1024
	ds_read_b128 v[208:211], v140 offset:2048
	ds_read_b128 v[212:215], v140 offset:3072
	v_lshl_add_u64 v[140:141], s[40:41], 0, v[194:195]
	s_mov_b32 m0, s54
	v_lshl_add_u64 v[216:217], s[40:41], 0, v[134:135]
	global_load_lds_dwordx4 v[140:141], off
	s_add_i32 m0, s54, 0x2000
	s_nop 0
	global_load_lds_dwordx4 v[216:217], off
	s_barrier
	s_waitcnt lgkmcnt(0)
	s_setprio 1
	s_waitcnt lgkmcnt(0)
	v_mfma_f32_16x16x32_bf16 v[114:117], v[200:203], v[162:165], 0
	v_mfma_f32_16x16x32_bf16 v[106:109], v[208:211], v[162:165], 0
	v_mfma_f32_16x16x32_bf16 v[98:101], v[200:203], v[170:173], 0
	v_mfma_f32_16x16x32_bf16 v[90:93], v[208:211], v[170:173], 0
	v_mfma_f32_16x16x32_bf16 v[82:85], v[200:203], v[178:181], 0
	v_mfma_f32_16x16x32_bf16 v[74:77], v[208:211], v[178:181], 0
	v_mfma_f32_16x16x32_bf16 v[70:73], v[200:203], v[186:189], 0
	v_mfma_f32_16x16x32_bf16 v[66:69], v[208:211], v[186:189], 0
	v_mfma_f32_16x16x32_bf16 v[114:117], v[204:207], v[166:169], v[114:117]
	v_mfma_f32_16x16x32_bf16 v[106:109], v[212:215], v[166:169], v[106:109]
	v_mfma_f32_16x16x32_bf16 v[98:101], v[204:207], v[174:177], v[98:101]
	v_mfma_f32_16x16x32_bf16 v[90:93], v[212:215], v[174:177], v[90:93]
	v_mfma_f32_16x16x32_bf16 v[82:85], v[204:207], v[182:185], v[82:85]
	v_mfma_f32_16x16x32_bf16 v[74:77], v[212:215], v[182:185], v[74:77]
	v_mfma_f32_16x16x32_bf16 v[70:73], v[204:207], v[190:193], v[70:73]
	v_mfma_f32_16x16x32_bf16 v[66:69], v[212:215], v[190:193], v[66:69]
	s_setprio 0
	s_mov_b32 m0, s14
	v_lshl_add_u64 v[220:221], s[42:43], 0, v[130:131]
	s_barrier
	ds_read_b128 v[162:165], v144 offset:16384
	ds_read_b128 v[166:169], v144 offset:17408
	ds_read_b128 v[170:173], v144 offset:18432
	ds_read_b128 v[174:177], v144 offset:19456
	ds_read_b128 v[178:181], v144 offset:20480
	ds_read_b128 v[182:185], v144 offset:21504
	ds_read_b128 v[186:189], v144 offset:22528
	ds_read_b128 v[190:193], v144 offset:23552
	global_load_lds_dwordx4 v[220:221], off
	v_lshl_add_u64 v[222:223], s[42:43], 0, v[132:133]
	s_mov_b32 m0, s16
	s_nop 0
	global_load_lds_dwordx4 v[222:223], off
	s_barrier
	s_waitcnt lgkmcnt(0)
	s_setprio 1
	s_waitcnt lgkmcnt(0)
	v_mfma_f32_16x16x32_bf16 v[62:65], v[146:149], v[162:165], 0
	v_mfma_f32_16x16x32_bf16 v[58:61], v[154:157], v[162:165], 0
	v_mfma_f32_16x16x32_bf16 v[54:57], v[146:149], v[170:173], 0
	v_mfma_f32_16x16x32_bf16 v[46:49], v[154:157], v[170:173], 0
	v_mfma_f32_16x16x32_bf16 v[38:41], v[146:149], v[178:181], 0
	v_mfma_f32_16x16x32_bf16 v[30:33], v[154:157], v[178:181], 0
	v_mfma_f32_16x16x32_bf16 v[22:25], v[146:149], v[186:189], 0
	v_mfma_f32_16x16x32_bf16 v[14:17], v[154:157], v[186:189], 0
	v_mfma_f32_16x16x32_bf16 v[62:65], v[150:153], v[166:169], v[62:65]
	v_mfma_f32_16x16x32_bf16 v[58:61], v[158:161], v[166:169], v[58:61]
	v_mfma_f32_16x16x32_bf16 v[54:57], v[150:153], v[174:177], v[54:57]
	v_mfma_f32_16x16x32_bf16 v[46:49], v[158:161], v[174:177], v[46:49]
	v_mfma_f32_16x16x32_bf16 v[38:41], v[150:153], v[182:185], v[38:41]
	v_mfma_f32_16x16x32_bf16 v[30:33], v[158:161], v[182:185], v[30:33]
	v_mfma_f32_16x16x32_bf16 v[22:25], v[150:153], v[190:193], v[22:25]
	v_mfma_f32_16x16x32_bf16 v[14:17], v[158:161], v[190:193], v[14:17]
	s_setprio 0
	s_barrier
	s_add_u32 s54, s40, 0x80000
	s_addc_u32 s55, s41, 0
	s_add_i32 s56, s56, s13
	v_lshl_add_u64 v[146:147], s[54:55], 0, v[194:195]
	s_mov_b32 m0, s56
	s_nop 0
	global_load_lds_dwordx4 v[146:147], off
	v_lshl_add_u64 v[146:147], s[54:55], 0, v[134:135]
	s_add_i32 m0, s56, 0x2000
	s_nop 0
	global_load_lds_dwordx4 v[146:147], off
	s_waitcnt vmcnt(6)
	s_barrier
	s_setprio 1
	v_mfma_f32_16x16x32_bf16 v[50:53], v[200:203], v[162:165], 0
	v_mfma_f32_16x16x32_bf16 v[42:45], v[208:211], v[162:165], 0
	v_mfma_f32_16x16x32_bf16 v[34:37], v[200:203], v[170:173], 0
	v_mfma_f32_16x16x32_bf16 v[26:29], v[208:211], v[170:173], 0
	v_mfma_f32_16x16x32_bf16 v[18:21], v[200:203], v[178:181], 0
	v_mfma_f32_16x16x32_bf16 v[10:13], v[208:211], v[178:181], 0
	v_mfma_f32_16x16x32_bf16 v[6:9], v[200:203], v[186:189], 0
	v_mfma_f32_16x16x32_bf16 v[2:5], v[208:211], v[186:189], 0
	v_mfma_f32_16x16x32_bf16 v[50:53], v[204:207], v[166:169], v[50:53]
	v_mfma_f32_16x16x32_bf16 v[42:45], v[212:215], v[166:169], v[42:45]
	v_mfma_f32_16x16x32_bf16 v[34:37], v[204:207], v[174:177], v[34:37]
	v_mfma_f32_16x16x32_bf16 v[26:29], v[212:215], v[174:177], v[26:29]
	v_mfma_f32_16x16x32_bf16 v[18:21], v[204:207], v[182:185], v[18:21]
	v_mfma_f32_16x16x32_bf16 v[10:13], v[212:215], v[182:185], v[10:13]
	v_mfma_f32_16x16x32_bf16 v[6:9], v[204:207], v[190:193], v[6:9]
	v_mfma_f32_16x16x32_bf16 v[2:5], v[212:215], v[190:193], v[2:5]
	s_setprio 0
	s_add_i32 s54, 0, 0x18000
	v_add_u32_e32 v145, s54, v142
	s_barrier
	ds_read_b128 v[146:149], v145
	ds_read_b128 v[150:153], v145 offset:1024
	ds_read_b128 v[154:157], v145 offset:2048
	ds_read_b128 v[158:161], v145 offset:3072
	s_add_u32 s42, s42, 0x80000
	s_addc_u32 s43, s43, 0
	s_mov_b32 m0, s17
	v_lshl_add_u64 v[200:201], s[42:43], 0, v[130:131]
	ds_read_b128 v[162:165], v144 offset:32768
	ds_read_b128 v[166:169], v144 offset:33792
	ds_read_b128 v[170:173], v144 offset:34816
	ds_read_b128 v[174:177], v144 offset:35840
	ds_read_b128 v[178:181], v144 offset:36864
	ds_read_b128 v[182:185], v144 offset:37888
	ds_read_b128 v[186:189], v144 offset:38912
	ds_read_b128 v[190:193], v144 offset:39936
	global_load_lds_dwordx4 v[200:201], off
	v_lshl_add_u64 v[200:201], s[42:43], 0, v[132:133]
	s_mov_b32 m0, s18
	s_nop 0
	global_load_lds_dwordx4 v[200:201], off
	s_waitcnt lgkmcnt(8)
	s_barrier
	s_waitcnt lgkmcnt(0)
	s_setprio 1
	s_waitcnt lgkmcnt(0)
	v_mfma_f32_16x16x32_bf16 v[126:129], v[146:149], v[162:165], v[126:129]
	v_mfma_f32_16x16x32_bf16 v[122:125], v[154:157], v[162:165], v[122:125]
	v_mfma_f32_16x16x32_bf16 v[118:121], v[146:149], v[170:173], v[118:121]
	v_mfma_f32_16x16x32_bf16 v[110:113], v[154:157], v[170:173], v[110:113]
	v_mfma_f32_16x16x32_bf16 v[102:105], v[146:149], v[178:181], v[102:105]
	v_mfma_f32_16x16x32_bf16 v[94:97], v[154:157], v[178:181], v[94:97]
	v_mfma_f32_16x16x32_bf16 v[86:89], v[146:149], v[186:189], v[86:89]
	v_mfma_f32_16x16x32_bf16 v[78:81], v[154:157], v[186:189], v[78:81]
	v_mfma_f32_16x16x32_bf16 v[126:129], v[150:153], v[166:169], v[126:129]
	v_mfma_f32_16x16x32_bf16 v[122:125], v[158:161], v[166:169], v[122:125]
	v_mfma_f32_16x16x32_bf16 v[118:121], v[150:153], v[174:177], v[118:121]
	v_mfma_f32_16x16x32_bf16 v[110:113], v[158:161], v[174:177], v[110:113]
	v_mfma_f32_16x16x32_bf16 v[102:105], v[150:153], v[182:185], v[102:105]
	v_mfma_f32_16x16x32_bf16 v[94:97], v[158:161], v[182:185], v[94:97]
	v_mfma_f32_16x16x32_bf16 v[86:89], v[150:153], v[190:193], v[86:89]
	v_mfma_f32_16x16x32_bf16 v[78:81], v[158:161], v[190:193], v[78:81]
	s_setprio 0
	s_barrier
	s_add_i32 s42, 0, 0x1c000
	s_add_i32 s43, s54, s13
	v_add_u32_e32 v145, s42, v142
	v_lshl_add_u64 v[140:141], v[140:141], 0, s[30:31]
	s_mov_b32 m0, s43
	ds_read_b128 v[200:203], v145
	ds_read_b128 v[204:207], v145 offset:1024
	ds_read_b128 v[208:211], v145 offset:2048
	ds_read_b128 v[212:215], v145 offset:3072
	global_load_lds_dwordx4 v[140:141], off
	v_lshl_add_u64 v[140:141], v[216:217], 0, s[30:31]
	s_add_i32 m0, s43, 0x2000
	s_nop 0
	global_load_lds_dwordx4 v[140:141], off
	s_barrier
	s_waitcnt lgkmcnt(0)
	s_setprio 1
	s_waitcnt lgkmcnt(0)
	v_mfma_f32_16x16x32_bf16 v[114:117], v[200:203], v[162:165], v[114:117]
	v_mfma_f32_16x16x32_bf16 v[106:109], v[208:211], v[162:165], v[106:109]
	v_mfma_f32_16x16x32_bf16 v[98:101], v[200:203], v[170:173], v[98:101]
	v_mfma_f32_16x16x32_bf16 v[90:93], v[208:211], v[170:173], v[90:93]
	v_mfma_f32_16x16x32_bf16 v[82:85], v[200:203], v[178:181], v[82:85]
	v_mfma_f32_16x16x32_bf16 v[74:77], v[208:211], v[178:181], v[74:77]
	v_mfma_f32_16x16x32_bf16 v[70:73], v[200:203], v[186:189], v[70:73]
	v_mfma_f32_16x16x32_bf16 v[66:69], v[208:211], v[186:189], v[66:69]
	v_mfma_f32_16x16x32_bf16 v[114:117], v[204:207], v[166:169], v[114:117]
	v_mfma_f32_16x16x32_bf16 v[106:109], v[212:215], v[166:169], v[106:109]
	v_mfma_f32_16x16x32_bf16 v[98:101], v[204:207], v[174:177], v[98:101]
	v_mfma_f32_16x16x32_bf16 v[90:93], v[212:215], v[174:177], v[90:93]
	v_mfma_f32_16x16x32_bf16 v[82:85], v[204:207], v[182:185], v[82:85]
	v_mfma_f32_16x16x32_bf16 v[74:77], v[212:215], v[182:185], v[74:77]
	v_mfma_f32_16x16x32_bf16 v[70:73], v[204:207], v[190:193], v[70:73]
	v_mfma_f32_16x16x32_bf16 v[66:69], v[212:215], v[190:193], v[66:69]
	s_setprio 0
	s_mov_b32 m0, s19
	v_lshl_add_u64 v[140:141], v[220:221], 0, s[30:31]
	s_barrier
	ds_read_b128 v[162:165], v144 offset:49152
	ds_read_b128 v[166:169], v144 offset:50176
	ds_read_b128 v[170:173], v144 offset:51200
	ds_read_b128 v[174:177], v144 offset:52224
	ds_read_b128 v[178:181], v144 offset:53248
	ds_read_b128 v[182:185], v144 offset:54272
	ds_read_b128 v[186:189], v144 offset:55296
	ds_read_b128 v[190:193], v144 offset:56320
	global_load_lds_dwordx4 v[140:141], off
	v_lshl_add_u64 v[140:141], v[222:223], 0, s[30:31]
	s_mov_b32 m0, s24
	s_nop 0
	global_load_lds_dwordx4 v[140:141], off
	s_barrier
	s_waitcnt lgkmcnt(0)
	s_setprio 1
	s_waitcnt lgkmcnt(0)
	v_mfma_f32_16x16x32_bf16 v[62:65], v[146:149], v[162:165], v[62:65]
	v_mfma_f32_16x16x32_bf16 v[58:61], v[154:157], v[162:165], v[58:61]
	v_mfma_f32_16x16x32_bf16 v[54:57], v[146:149], v[170:173], v[54:57]
	v_mfma_f32_16x16x32_bf16 v[46:49], v[154:157], v[170:173], v[46:49]
	v_mfma_f32_16x16x32_bf16 v[38:41], v[146:149], v[178:181], v[38:41]
	v_mfma_f32_16x16x32_bf16 v[30:33], v[154:157], v[178:181], v[30:33]
	v_mfma_f32_16x16x32_bf16 v[22:25], v[146:149], v[186:189], v[22:25]
	v_mfma_f32_16x16x32_bf16 v[14:17], v[154:157], v[186:189], v[14:17]
	v_mfma_f32_16x16x32_bf16 v[62:65], v[150:153], v[166:169], v[62:65]
	v_mfma_f32_16x16x32_bf16 v[58:61], v[158:161], v[166:169], v[58:61]
	v_mfma_f32_16x16x32_bf16 v[54:57], v[150:153], v[174:177], v[54:57]
	v_mfma_f32_16x16x32_bf16 v[46:49], v[158:161], v[174:177], v[46:49]
	v_mfma_f32_16x16x32_bf16 v[38:41], v[150:153], v[182:185], v[38:41]
	v_mfma_f32_16x16x32_bf16 v[30:33], v[158:161], v[182:185], v[30:33]
	v_mfma_f32_16x16x32_bf16 v[22:25], v[150:153], v[190:193], v[22:25]
	v_mfma_f32_16x16x32_bf16 v[14:17], v[158:161], v[190:193], v[14:17]
	s_setprio 0
	s_barrier
	s_add_u32 s40, s40, 0x80080
	s_addc_u32 s41, s41, 0
	s_add_i32 s42, s42, s13
	v_lshl_add_u64 v[140:141], s[40:41], 0, v[194:195]
	s_mov_b32 m0, s42
	s_nop 0
	global_load_lds_dwordx4 v[140:141], off
	v_lshl_add_u64 v[140:141], s[40:41], 0, v[134:135]
	s_add_i32 m0, s42, 0x2000
	s_nop 0
	global_load_lds_dwordx4 v[140:141], off
	s_waitcnt vmcnt(6)
	s_barrier
	s_setprio 1
	v_mfma_f32_16x16x32_bf16 v[50:53], v[200:203], v[162:165], v[50:53]
	v_mfma_f32_16x16x32_bf16 v[42:45], v[208:211], v[162:165], v[42:45]
	v_mfma_f32_16x16x32_bf16 v[34:37], v[200:203], v[170:173], v[34:37]
	v_mfma_f32_16x16x32_bf16 v[26:29], v[208:211], v[170:173], v[26:29]
	v_mfma_f32_16x16x32_bf16 v[18:21], v[200:203], v[178:181], v[18:21]
	v_mfma_f32_16x16x32_bf16 v[10:13], v[208:211], v[178:181], v[10:13]
	v_mfma_f32_16x16x32_bf16 v[6:9], v[200:203], v[186:189], v[6:9]
	v_mfma_f32_16x16x32_bf16 v[2:5], v[208:211], v[186:189], v[2:5]
	v_mfma_f32_16x16x32_bf16 v[50:53], v[204:207], v[166:169], v[50:53]
	v_mfma_f32_16x16x32_bf16 v[42:45], v[212:215], v[166:169], v[42:45]
	v_mfma_f32_16x16x32_bf16 v[34:37], v[204:207], v[174:177], v[34:37]
	v_mfma_f32_16x16x32_bf16 v[26:29], v[212:215], v[174:177], v[26:29]
	v_mfma_f32_16x16x32_bf16 v[18:21], v[204:207], v[182:185], v[18:21]
	v_mfma_f32_16x16x32_bf16 v[10:13], v[212:215], v[182:185], v[10:13]
	v_mfma_f32_16x16x32_bf16 v[6:9], v[204:207], v[190:193], v[6:9]
	v_mfma_f32_16x16x32_bf16 v[2:5], v[212:215], v[190:193], v[2:5]
	s_setprio 0
	s_add_i32 s53, s53, 2
	s_add_u32 s38, s38, 0x100
	s_addc_u32 s39, s39, 0
	s_add_u32 s51, s51, 0x100
	s_addc_u32 s52, s52, 0
	s_cmp_gt_u32 s53, 29
	s_barrier
	s_cbranch_scc1 .Lpk683_exit

.Lpk683_exit:
	v_add_u32_e32 v140, s35, v1
	v_ashrrev_i32_e32 v141, 31, v140
	v_add_u32_e32 v146, s33, v143
	v_lshlrev_b64 v[140:141], 12, v[140:141]
	v_ashrrev_i32_e32 v147, 31, v146
	v_lshl_add_u64 v[140:141], s[4:5], 0, v[140:141]
	v_lshl_add_u64 v[140:141], v[146:147], 1, v[140:141]
	s_mov_b32 s33, 0x10000
	v_cvt_pk_bf16_f32 v126, v126, v127
	v_cvt_pk_bf16_f32 v127, v128, v129
	v_cvt_pk_bf16_f32 v128, v122, v123
	v_cvt_pk_bf16_f32 v129, v124, v125
	global_store_dwordx4 v[140:141], v[126:129], off
	v_cvt_pk_bf16_f32 v114, v114, v115
	v_cvt_pk_bf16_f32 v115, v116, v117
	v_cvt_pk_bf16_f32 v116, v106, v107
	v_cvt_pk_bf16_f32 v117, v108, v109
	global_store_dwordx4 v[140:141], v[114:117], off offset:256
	s_mov_b64 s[38:39], 0x10000
	v_cvt_pk_bf16_f32 v106, v118, v119
	v_cvt_pk_bf16_f32 v107, v120, v121
	v_cvt_pk_bf16_f32 v108, v110, v111
	v_add_co_u32_e32 v110, vcc, s33, v140
	v_lshl_add_u64 v[114:115], v[140:141], 0, s[38:39]
	s_nop 0
	v_addc_co_u32_e32 v111, vcc, 0, v141, vcc
	s_mov_b32 s33, 0x20000
	v_cvt_pk_bf16_f32 v109, v112, v113
	global_store_dwordx4 v[110:111], v[106:109], off
	v_cvt_pk_bf16_f32 v98, v98, v99
	v_cvt_pk_bf16_f32 v99, v100, v101
	v_cvt_pk_bf16_f32 v100, v90, v91
	v_cvt_pk_bf16_f32 v101, v92, v93
	global_store_dwordx4 v[114:115], v[98:101], off offset:256
	s_mov_b64 s[38:39], 0x20000
	v_cvt_pk_bf16_f32 v90, v102, v103
	v_cvt_pk_bf16_f32 v91, v104, v105
	v_cvt_pk_bf16_f32 v92, v94, v95
	v_add_co_u32_e32 v94, vcc, s33, v140
	v_lshl_add_u64 v[98:99], v[140:141], 0, s[38:39]
	s_nop 0
	v_addc_co_u32_e32 v95, vcc, 0, v141, vcc
	s_mov_b32 s33, 0x30000
	v_cvt_pk_bf16_f32 v93, v96, v97
	global_store_dwordx4 v[94:95], v[90:93], off
	v_cvt_pk_bf16_f32 v82, v82, v83
	v_cvt_pk_bf16_f32 v83, v84, v85
	v_cvt_pk_bf16_f32 v84, v74, v75
	v_cvt_pk_bf16_f32 v85, v76, v77
	global_store_dwordx4 v[98:99], v[82:85], off offset:256
	s_mov_b64 s[38:39], 0x30000
	v_cvt_pk_bf16_f32 v74, v86, v87
	v_cvt_pk_bf16_f32 v75, v88, v89
	v_cvt_pk_bf16_f32 v76, v78, v79
	v_add_co_u32_e32 v78, vcc, s33, v140
	v_lshl_add_u64 v[82:83], v[140:141], 0, s[38:39]
	s_nop 0
	v_addc_co_u32_e32 v79, vcc, 0, v141, vcc
	s_mov_b32 s33, 0x80000
	v_cvt_pk_bf16_f32 v77, v80, v81
	global_store_dwordx4 v[78:79], v[74:77], off
	v_cvt_pk_bf16_f32 v70, v70, v71
	v_cvt_pk_bf16_f32 v71, v72, v73
	v_cvt_pk_bf16_f32 v72, v66, v67
	v_cvt_pk_bf16_f32 v73, v68, v69
	global_store_dwordx4 v[82:83], v[70:73], off offset:256
	s_mov_b64 s[38:39], 0x80000
	v_cvt_pk_bf16_f32 v62, v62, v63
	v_cvt_pk_bf16_f32 v63, v64, v65
	v_cvt_pk_bf16_f32 v64, v58, v59
	v_add_co_u32_e32 v58, vcc, s33, v140
	v_lshl_add_u64 v[66:67], v[140:141], 0, s[38:39]
	s_nop 0
	v_addc_co_u32_e32 v59, vcc, 0, v141, vcc
	s_mov_b32 s33, 0x90000
	v_cvt_pk_bf16_f32 v65, v60, v61
	global_store_dwordx4 v[58:59], v[62:65], off
	v_cvt_pk_bf16_f32 v50, v50, v51
	v_cvt_pk_bf16_f32 v51, v52, v53
	v_cvt_pk_bf16_f32 v52, v42, v43
	v_cvt_pk_bf16_f32 v53, v44, v45
	global_store_dwordx4 v[66:67], v[50:53], off offset:256
	s_mov_b64 s[38:39], 0x90000
	v_cvt_pk_bf16_f32 v42, v54, v55
	v_cvt_pk_bf16_f32 v43, v56, v57
	v_cvt_pk_bf16_f32 v44, v46, v47
	v_add_co_u32_e32 v46, vcc, s33, v140
	v_lshl_add_u64 v[50:51], v[140:141], 0, s[38:39]
	s_nop 0
	v_addc_co_u32_e32 v47, vcc, 0, v141, vcc
	s_mov_b32 s33, 0xa0000
	v_cvt_pk_bf16_f32 v45, v48, v49
	global_store_dwordx4 v[46:47], v[42:45], off
	v_cvt_pk_bf16_f32 v34, v34, v35
	v_cvt_pk_bf16_f32 v35, v36, v37
	v_cvt_pk_bf16_f32 v36, v26, v27
	v_cvt_pk_bf16_f32 v37, v28, v29
	global_store_dwordx4 v[50:51], v[34:37], off offset:256
	s_mov_b64 s[38:39], 0xa0000
	v_cvt_pk_bf16_f32 v26, v38, v39
	v_cvt_pk_bf16_f32 v27, v40, v41
	v_cvt_pk_bf16_f32 v28, v30, v31
	v_add_co_u32_e32 v30, vcc, s33, v140
	v_lshl_add_u64 v[34:35], v[140:141], 0, s[38:39]
	s_nop 0
	v_addc_co_u32_e32 v31, vcc, 0, v141, vcc
	s_mov_b32 s33, 0xb0000
	v_cvt_pk_bf16_f32 v29, v32, v33
	global_store_dwordx4 v[30:31], v[26:29], off
	v_cvt_pk_bf16_f32 v18, v18, v19
	v_cvt_pk_bf16_f32 v19, v20, v21
	v_cvt_pk_bf16_f32 v20, v10, v11
	v_cvt_pk_bf16_f32 v21, v12, v13
	global_store_dwordx4 v[34:35], v[18:21], off offset:256
	v_cvt_pk_bf16_f32 v10, v22, v23
	v_cvt_pk_bf16_f32 v11, v24, v25
	v_cvt_pk_bf16_f32 v12, v14, v15
	v_add_co_u32_e32 v14, vcc, s33, v140
	s_mov_b64 s[38:39], 0xb0000
	s_nop 0
	v_addc_co_u32_e32 v15, vcc, 0, v141, vcc
	v_lshl_add_u64 v[18:19], v[140:141], 0, s[38:39]
	s_and_b64 vcc, exec, s[6:7]
	s_mov_b32 s33, s9
	s_mov_b32 s35, s8
	s_mov_b64 s[40:41], s[36:37]
	s_mov_b64 s[38:39], s[28:29]
	v_cvt_pk_bf16_f32 v13, v16, v17
	global_store_dwordx4 v[14:15], v[10:13], off
	v_cvt_pk_bf16_f32 v6, v6, v7
	v_cvt_pk_bf16_f32 v7, v8, v9
	v_cvt_pk_bf16_f32 v8, v2, v3
	v_cvt_pk_bf16_f32 v9, v4, v5
	global_store_dwordx4 v[18:19], v[6:9], off offset:256
	s_cbranch_vccz .LBB0_676
	s_waitcnt vmcnt(0)
	s_cmpk_gt_u32 s10, 0xff
	s_cbranch_scc1 .LBB0_687
	s_barrier

.LBB0_704:
	s_add_u32 s28, s2, s22
	s_addc_u32 s29, s44, s23
	s_and_b64 s[36:37], s[42:43], exec
	s_cselect_b32 s47, s29, s39
	s_cselect_b32 s48, s28, s38
	s_add_u32 s36, s45, s26
	s_addc_u32 s37, s46, s27
	s_and_b64 s[42:43], s[42:43], exec
	s_cselect_b32 s49, s37, s41
	s_cselect_b32 s50, s36, s40
	s_add_u32 s38, s38, 0x40080
	s_addc_u32 s39, s39, 0
	s_add_u32 s51, s40, 0x100
	s_addc_u32 s52, s41, 0
	s_mov_b32 s53, -2
	s_add_u32 s40, s38, 0xfffc0080
	s_addc_u32 s41, s39, -1
	s_add_i32 s55, 0, 0x10000
	v_add_u32_e32 v14, s55, v182
	ds_read_b128 v[2:5], v14
	ds_read_b128 v[6:9], v14 offset:1024
	ds_read_b128 v[10:13], v14 offset:2048
	ds_read_b128 v[14:17], v14 offset:3072
	s_cmp_eq_u32 s53, 12
	s_cselect_b32 s43, s47, s41
	s_cselect_b32 s42, s48, s40
	s_cselect_b32 s41, s49, s52
	s_cselect_b32 s40, s50, s51
	v_lshl_add_u64 v[18:19], s[38:39], 0, v[168:169]
	s_add_i32 m0, s14, 0xc000
	ds_read_b128 v[186:189], v184
	ds_read_b128 v[190:193], v184 offset:1024
	ds_read_b128 v[200:203], v184 offset:2048
	ds_read_b128 v[204:207], v184 offset:3072
	ds_read_b128 v[208:211], v184 offset:4096
	ds_read_b128 v[212:215], v184 offset:5120
	ds_read_b128 v[232:235], v184 offset:6144
	ds_read_b128 v[236:239], v184 offset:7168
	global_load_lds_dwordx4 v[18:19], off
	v_lshl_add_u64 v[18:19], s[38:39], 0, v[170:171]
	s_add_i32 m0, s14, 0xe000
	s_nop 0
	global_load_lds_dwordx4 v[18:19], off
	s_waitcnt lgkmcnt(8)
	s_barrier
	s_waitcnt lgkmcnt(0)
	s_setprio 1
	s_waitcnt lgkmcnt(0)
	v_mfma_scale_f32_16x16x128_f8f6f4 v[158:161], v[2:9], v[186:193], 0, v1, v180 op_sel_hi:[0,0,0]
	v_mfma_scale_f32_16x16x128_f8f6f4 v[154:157], v[10:17], v[186:193], 0, v1, v180 op_sel_hi:[0,0,0]
	v_mfma_scale_f32_16x16x128_f8f6f4 v[150:153], v[2:9], v[200:207], 0, v1, v180 op_sel_hi:[0,0,0]
	v_mfma_scale_f32_16x16x128_f8f6f4 v[142:145], v[10:17], v[200:207], 0, v1, v180 op_sel_hi:[0,0,0]
	v_mfma_scale_f32_16x16x128_f8f6f4 v[134:137], v[2:9], v[208:215], 0, v1, v180 op_sel_hi:[0,0,0]
	v_mfma_scale_f32_16x16x128_f8f6f4 v[126:129], v[10:17], v[208:215], 0, v1, v180 op_sel_hi:[0,0,0]
	v_mfma_scale_f32_16x16x128_f8f6f4 v[118:121], v[2:9], v[232:239], 0, v1, v180 op_sel_hi:[0,0,0]
	v_mfma_scale_f32_16x16x128_f8f6f4 v[110:113], v[10:17], v[232:239], 0, v1, v180 op_sel_hi:[0,0,0]
	s_setprio 0
	s_barrier
	s_add_i32 s54, 0, 0x14000
	s_add_i32 s55, s55, s13
	v_add_u32_e32 v30, s54, v182
	v_lshl_add_u64 v[172:173], s[40:41], 0, v[194:195]
	s_mov_b32 m0, s55
	ds_read_b128 v[18:21], v30
	ds_read_b128 v[22:25], v30 offset:1024
	ds_read_b128 v[26:29], v30 offset:2048
	ds_read_b128 v[30:33], v30 offset:3072
	global_load_lds_dwordx4 v[172:173], off
	v_lshl_add_u64 v[174:175], s[40:41], 0, v[166:167]
	s_add_i32 m0, s55, 0x2000
	s_nop 0
	global_load_lds_dwordx4 v[174:175], off
	s_barrier
	s_waitcnt lgkmcnt(0)
	s_setprio 1
	s_waitcnt lgkmcnt(0)
	v_mfma_scale_f32_16x16x128_f8f6f4 v[146:149], v[18:25], v[186:193], 0, v1, v180 op_sel_hi:[0,0,0]
	v_mfma_scale_f32_16x16x128_f8f6f4 v[138:141], v[26:33], v[186:193], 0, v1, v180 op_sel_hi:[0,0,0]
	v_mfma_scale_f32_16x16x128_f8f6f4 v[130:133], v[18:25], v[200:207], 0, v1, v180 op_sel_hi:[0,0,0]
	v_mfma_scale_f32_16x16x128_f8f6f4 v[122:125], v[26:33], v[200:207], 0, v1, v180 op_sel_hi:[0,0,0]
	v_mfma_scale_f32_16x16x128_f8f6f4 v[114:117], v[18:25], v[208:215], 0, v1, v180 op_sel_hi:[0,0,0]
	v_mfma_scale_f32_16x16x128_f8f6f4 v[106:109], v[26:33], v[208:215], 0, v1, v180 op_sel_hi:[0,0,0]
	v_mfma_scale_f32_16x16x128_f8f6f4 v[102:105], v[18:25], v[232:239], 0, v1, v180 op_sel_hi:[0,0,0]
	v_mfma_scale_f32_16x16x128_f8f6f4 v[98:101], v[26:33], v[232:239], 0, v1, v180 op_sel_hi:[0,0,0]
	s_setprio 0
	s_mov_b32 m0, s14
	v_lshl_add_u64 v[176:177], s[42:43], 0, v[162:163]
	s_barrier
	ds_read_b128 v[186:189], v184 offset:16384
	ds_read_b128 v[190:193], v184 offset:17408
	ds_read_b128 v[200:203], v184 offset:18432
	ds_read_b128 v[204:207], v184 offset:19456
	ds_read_b128 v[208:211], v184 offset:20480
	ds_read_b128 v[212:215], v184 offset:21504
	ds_read_b128 v[232:235], v184 offset:22528
	ds_read_b128 v[236:239], v184 offset:23552
	global_load_lds_dwordx4 v[176:177], off
	v_lshl_add_u64 v[178:179], s[42:43], 0, v[164:165]
	s_mov_b32 m0, s16
	s_nop 0
	global_load_lds_dwordx4 v[178:179], off
	s_barrier
	s_waitcnt lgkmcnt(0)
	s_setprio 1
	s_waitcnt lgkmcnt(0)
	v_mfma_scale_f32_16x16x128_f8f6f4 v[94:97], v[2:9], v[186:193], 0, v1, v180 op_sel_hi:[0,0,0]
	v_mfma_scale_f32_16x16x128_f8f6f4 v[90:93], v[10:17], v[186:193], 0, v1, v180 op_sel_hi:[0,0,0]
	v_mfma_scale_f32_16x16x128_f8f6f4 v[86:89], v[2:9], v[200:207], 0, v1, v180 op_sel_hi:[0,0,0]
	v_mfma_scale_f32_16x16x128_f8f6f4 v[78:81], v[10:17], v[200:207], 0, v1, v180 op_sel_hi:[0,0,0]
	v_mfma_scale_f32_16x16x128_f8f6f4 v[70:73], v[2:9], v[208:215], 0, v1, v180 op_sel_hi:[0,0,0]
	v_mfma_scale_f32_16x16x128_f8f6f4 v[62:65], v[10:17], v[208:215], 0, v1, v180 op_sel_hi:[0,0,0]
	v_mfma_scale_f32_16x16x128_f8f6f4 v[54:57], v[2:9], v[232:239], 0, v1, v180 op_sel_hi:[0,0,0]
	v_mfma_scale_f32_16x16x128_f8f6f4 v[46:49], v[10:17], v[232:239], 0, v1, v180 op_sel_hi:[0,0,0]
	s_setprio 0
	s_barrier
	s_add_u32 s56, s40, 0x40000
	s_addc_u32 s57, s41, 0
	s_add_i32 s54, s54, s13
	v_lshl_add_u64 v[2:3], s[56:57], 0, v[194:195]
	s_mov_b32 m0, s54
	s_nop 0
	global_load_lds_dwordx4 v[2:3], off
	v_lshl_add_u64 v[2:3], s[56:57], 0, v[166:167]
	s_add_i32 m0, s54, 0x2000
	s_nop 0
	global_load_lds_dwordx4 v[2:3], off
	s_waitcnt vmcnt(6)
	s_barrier
	s_setprio 1
	v_mfma_scale_f32_16x16x128_f8f6f4 v[82:85], v[18:25], v[186:193], 0, v1, v180 op_sel_hi:[0,0,0]
	v_mfma_scale_f32_16x16x128_f8f6f4 v[74:77], v[26:33], v[186:193], 0, v1, v180 op_sel_hi:[0,0,0]
	v_mfma_scale_f32_16x16x128_f8f6f4 v[66:69], v[18:25], v[200:207], 0, v1, v180 op_sel_hi:[0,0,0]
	v_mfma_scale_f32_16x16x128_f8f6f4 v[58:61], v[26:33], v[200:207], 0, v1, v180 op_sel_hi:[0,0,0]
	v_mfma_scale_f32_16x16x128_f8f6f4 v[50:53], v[18:25], v[208:215], 0, v1, v180 op_sel_hi:[0,0,0]
	v_mfma_scale_f32_16x16x128_f8f6f4 v[42:45], v[26:33], v[208:215], 0, v1, v180 op_sel_hi:[0,0,0]
	v_mfma_scale_f32_16x16x128_f8f6f4 v[38:41], v[18:25], v[232:239], 0, v1, v180 op_sel_hi:[0,0,0]
	v_mfma_scale_f32_16x16x128_f8f6f4 v[34:37], v[26:33], v[232:239], 0, v1, v180 op_sel_hi:[0,0,0]
	s_setprio 0
	s_add_i32 s54, 0, 0x18000
	v_add_u32_e32 v14, s54, v182
	s_barrier
	ds_read_b128 v[2:5], v14
	ds_read_b128 v[6:9], v14 offset:1024
	ds_read_b128 v[10:13], v14 offset:2048
	ds_read_b128 v[14:17], v14 offset:3072
	s_add_u32 s42, s42, 0x40000
	s_addc_u32 s43, s43, 0
	s_mov_b32 m0, s17
	v_lshl_add_u64 v[208:209], s[42:43], 0, v[162:163]
	ds_read_b128 v[18:21], v184 offset:32768
	ds_read_b128 v[22:25], v184 offset:33792
	ds_read_b128 v[26:29], v184 offset:34816
	ds_read_b128 v[30:33], v184 offset:35840
	ds_read_b128 v[186:189], v184 offset:36864
	ds_read_b128 v[190:193], v184 offset:37888
	ds_read_b128 v[200:203], v184 offset:38912
	ds_read_b128 v[204:207], v184 offset:39936
	global_load_lds_dwordx4 v[208:209], off
	v_lshl_add_u64 v[208:209], s[42:43], 0, v[164:165]
	s_mov_b32 m0, s18
	s_nop 0
	global_load_lds_dwordx4 v[208:209], off
	s_waitcnt lgkmcnt(8)
	s_barrier
	s_waitcnt lgkmcnt(0)
	s_setprio 1
	s_waitcnt lgkmcnt(0)
	v_mfma_scale_f32_16x16x128_f8f6f4 v[158:161], v[2:9], v[18:25], v[158:161], v1, v180 op_sel_hi:[0,0,0]
	v_mfma_scale_f32_16x16x128_f8f6f4 v[154:157], v[10:17], v[18:25], v[154:157], v1, v180 op_sel_hi:[0,0,0]
	v_mfma_scale_f32_16x16x128_f8f6f4 v[150:153], v[2:9], v[26:33], v[150:153], v1, v180 op_sel_hi:[0,0,0]
	v_mfma_scale_f32_16x16x128_f8f6f4 v[142:145], v[10:17], v[26:33], v[142:145], v1, v180 op_sel_hi:[0,0,0]
	v_mfma_scale_f32_16x16x128_f8f6f4 v[134:137], v[2:9], v[186:193], v[134:137], v1, v180 op_sel_hi:[0,0,0]
	v_mfma_scale_f32_16x16x128_f8f6f4 v[126:129], v[10:17], v[186:193], v[126:129], v1, v180 op_sel_hi:[0,0,0]
	v_mfma_scale_f32_16x16x128_f8f6f4 v[118:121], v[2:9], v[200:207], v[118:121], v1, v180 op_sel_hi:[0,0,0]
	v_mfma_scale_f32_16x16x128_f8f6f4 v[110:113], v[10:17], v[200:207], v[110:113], v1, v180 op_sel_hi:[0,0,0]
	s_setprio 0
	s_barrier
	s_add_i32 s42, 0, 0x1c000
	s_add_i32 s43, s54, s13
	v_add_u32_e32 v185, s42, v182
	v_lshl_add_u64 v[172:173], v[172:173], 0, s[30:31]
	s_mov_b32 m0, s43
	ds_read_b128 v[208:211], v185
	ds_read_b128 v[212:215], v185 offset:1024
	ds_read_b128 v[232:235], v185 offset:2048
	ds_read_b128 v[236:239], v185 offset:3072
	global_load_lds_dwordx4 v[172:173], off
	v_lshl_add_u64 v[172:173], v[174:175], 0, s[30:31]
	s_add_i32 m0, s43, 0x2000
	s_nop 0
	global_load_lds_dwordx4 v[172:173], off
	s_barrier
	s_waitcnt lgkmcnt(0)
	s_setprio 1
	s_waitcnt lgkmcnt(0)
	v_mfma_scale_f32_16x16x128_f8f6f4 v[146:149], v[208:215], v[18:25], v[146:149], v1, v180 op_sel_hi:[0,0,0]
	v_mfma_scale_f32_16x16x128_f8f6f4 v[138:141], v[232:239], v[18:25], v[138:141], v1, v180 op_sel_hi:[0,0,0]
	v_mfma_scale_f32_16x16x128_f8f6f4 v[130:133], v[208:215], v[26:33], v[130:133], v1, v180 op_sel_hi:[0,0,0]
	v_mfma_scale_f32_16x16x128_f8f6f4 v[122:125], v[232:239], v[26:33], v[122:125], v1, v180 op_sel_hi:[0,0,0]
	v_mfma_scale_f32_16x16x128_f8f6f4 v[114:117], v[208:215], v[186:193], v[114:117], v1, v180 op_sel_hi:[0,0,0]
	v_mfma_scale_f32_16x16x128_f8f6f4 v[106:109], v[232:239], v[186:193], v[106:109], v1, v180 op_sel_hi:[0,0,0]
	v_mfma_scale_f32_16x16x128_f8f6f4 v[102:105], v[208:215], v[200:207], v[102:105], v1, v180 op_sel_hi:[0,0,0]
	v_mfma_scale_f32_16x16x128_f8f6f4 v[98:101], v[232:239], v[200:207], v[98:101], v1, v180 op_sel_hi:[0,0,0]
	s_setprio 0
	s_mov_b32 m0, s19
	v_lshl_add_u64 v[172:173], v[176:177], 0, s[30:31]
	s_barrier
	ds_read_b128 v[18:21], v184 offset:49152
	ds_read_b128 v[22:25], v184 offset:50176
	ds_read_b128 v[26:29], v184 offset:51200
	ds_read_b128 v[30:33], v184 offset:52224
	ds_read_b128 v[186:189], v184 offset:53248
	ds_read_b128 v[190:193], v184 offset:54272
	ds_read_b128 v[200:203], v184 offset:55296
	ds_read_b128 v[204:207], v184 offset:56320
	global_load_lds_dwordx4 v[172:173], off
	v_lshl_add_u64 v[172:173], v[178:179], 0, s[30:31]
	s_mov_b32 m0, s24
	s_nop 0
	global_load_lds_dwordx4 v[172:173], off
	s_barrier
	s_waitcnt lgkmcnt(0)
	s_setprio 1
	s_waitcnt lgkmcnt(0)
	v_mfma_scale_f32_16x16x128_f8f6f4 v[94:97], v[2:9], v[18:25], v[94:97], v1, v180 op_sel_hi:[0,0,0]
	v_mfma_scale_f32_16x16x128_f8f6f4 v[90:93], v[10:17], v[18:25], v[90:93], v1, v180 op_sel_hi:[0,0,0]
	v_mfma_scale_f32_16x16x128_f8f6f4 v[86:89], v[2:9], v[26:33], v[86:89], v1, v180 op_sel_hi:[0,0,0]
	v_mfma_scale_f32_16x16x128_f8f6f4 v[78:81], v[10:17], v[26:33], v[78:81], v1, v180 op_sel_hi:[0,0,0]
	v_mfma_scale_f32_16x16x128_f8f6f4 v[70:73], v[2:9], v[186:193], v[70:73], v1, v180 op_sel_hi:[0,0,0]
	v_mfma_scale_f32_16x16x128_f8f6f4 v[62:65], v[10:17], v[186:193], v[62:65], v1, v180 op_sel_hi:[0,0,0]
	v_mfma_scale_f32_16x16x128_f8f6f4 v[54:57], v[2:9], v[200:207], v[54:57], v1, v180 op_sel_hi:[0,0,0]
	v_mfma_scale_f32_16x16x128_f8f6f4 v[46:49], v[10:17], v[200:207], v[46:49], v1, v180 op_sel_hi:[0,0,0]
	s_setprio 0
	s_barrier
	s_add_u32 s40, s40, 0x40080
	s_addc_u32 s41, s41, 0
	s_add_i32 s42, s42, s13
	v_lshl_add_u64 v[2:3], s[40:41], 0, v[194:195]
	s_mov_b32 m0, s42
	s_nop 0
	global_load_lds_dwordx4 v[2:3], off
	v_lshl_add_u64 v[2:3], s[40:41], 0, v[166:167]
	s_add_i32 m0, s42, 0x2000
	s_nop 0
	global_load_lds_dwordx4 v[2:3], off
	s_waitcnt vmcnt(6)
	s_barrier
	s_setprio 1
	v_mfma_scale_f32_16x16x128_f8f6f4 v[82:85], v[208:215], v[18:25], v[82:85], v1, v180 op_sel_hi:[0,0,0]
	v_mfma_scale_f32_16x16x128_f8f6f4 v[74:77], v[232:239], v[18:25], v[74:77], v1, v180 op_sel_hi:[0,0,0]
	v_mfma_scale_f32_16x16x128_f8f6f4 v[66:69], v[208:215], v[26:33], v[66:69], v1, v180 op_sel_hi:[0,0,0]
	v_mfma_scale_f32_16x16x128_f8f6f4 v[58:61], v[232:239], v[26:33], v[58:61], v1, v180 op_sel_hi:[0,0,0]
	v_mfma_scale_f32_16x16x128_f8f6f4 v[50:53], v[208:215], v[186:193], v[50:53], v1, v180 op_sel_hi:[0,0,0]
	v_mfma_scale_f32_16x16x128_f8f6f4 v[42:45], v[232:239], v[186:193], v[42:45], v1, v180 op_sel_hi:[0,0,0]
	v_mfma_scale_f32_16x16x128_f8f6f4 v[38:41], v[208:215], v[200:207], v[38:41], v1, v180 op_sel_hi:[0,0,0]
	v_mfma_scale_f32_16x16x128_f8f6f4 v[34:37], v[232:239], v[200:207], v[34:37], v1, v180 op_sel_hi:[0,0,0]
	s_setprio 0
	s_add_i32 s53, s53, 2
	s_add_u32 s38, s38, 0x100
	s_addc_u32 s39, s39, 0
	s_add_u32 s51, s51, 0x100
	s_addc_u32 s52, s52, 0
	s_cmp_gt_u32 s53, 13
	s_barrier
	s_cbranch_scc1 .Lpk705_exit

.Lpk705_exit:
	v_add_u32_e32 v2, s35, v181
	v_ashrrev_i32_e32 v3, 31, v2
	v_add_u32_e32 v4, s33, v183
	v_lshlrev_b64 v[2:3], 12, v[2:3]
	v_ashrrev_i32_e32 v5, 31, v4
	v_lshl_add_u64 v[2:3], s[4:5], 0, v[2:3]
	s_nop 15
	s_nop 15
	v_lshl_add_u64 v[2:3], v[4:5], 1, v[2:3]
	v_cvt_pk_bf16_f32 v4, v158, v159
	v_cvt_pk_bf16_f32 v5, v160, v161
	v_cvt_pk_bf16_f32 v6, v154, v155
	v_cvt_pk_bf16_f32 v7, v156, v157
	s_mov_b32 s33, 0x10000
	global_store_dwordx4 v[2:3], v[4:7], off
	v_add_co_u32_e32 v10, vcc, s33, v2
	s_nop 0
	v_cvt_pk_bf16_f32 v4, v146, v147
	v_cvt_pk_bf16_f32 v5, v148, v149
	v_cvt_pk_bf16_f32 v6, v138, v139
	v_cvt_pk_bf16_f32 v7, v140, v141
	global_store_dwordx4 v[2:3], v[4:7], off offset:256
	s_mov_b64 s[38:39], 0x10000
	v_addc_co_u32_e32 v11, vcc, 0, v3, vcc
	v_cvt_pk_bf16_f32 v4, v150, v151
	v_cvt_pk_bf16_f32 v5, v152, v153
	v_cvt_pk_bf16_f32 v6, v142, v143
	v_cvt_pk_bf16_f32 v7, v144, v145
	s_mov_b32 s33, 0x20000
	v_lshl_add_u64 v[8:9], v[2:3], 0, s[38:39]
	global_store_dwordx4 v[10:11], v[4:7], off
	v_add_co_u32_e32 v10, vcc, s33, v2
	s_nop 0
	v_cvt_pk_bf16_f32 v4, v130, v131
	v_cvt_pk_bf16_f32 v5, v132, v133
	v_cvt_pk_bf16_f32 v6, v122, v123
	v_cvt_pk_bf16_f32 v7, v124, v125
	global_store_dwordx4 v[8:9], v[4:7], off offset:256
	s_mov_b64 s[38:39], 0x20000
	v_addc_co_u32_e32 v11, vcc, 0, v3, vcc
	v_cvt_pk_bf16_f32 v4, v134, v135
	v_cvt_pk_bf16_f32 v5, v136, v137
	v_cvt_pk_bf16_f32 v6, v126, v127
	v_cvt_pk_bf16_f32 v7, v128, v129
	s_mov_b32 s33, 0x30000
	v_lshl_add_u64 v[8:9], v[2:3], 0, s[38:39]
	global_store_dwordx4 v[10:11], v[4:7], off
	v_add_co_u32_e32 v10, vcc, s33, v2
	s_nop 0
	v_cvt_pk_bf16_f32 v4, v114, v115
	v_cvt_pk_bf16_f32 v5, v116, v117
	v_cvt_pk_bf16_f32 v6, v106, v107
	v_cvt_pk_bf16_f32 v7, v108, v109
	global_store_dwordx4 v[8:9], v[4:7], off offset:256
	s_mov_b64 s[38:39], 0x30000
	v_addc_co_u32_e32 v11, vcc, 0, v3, vcc
	v_cvt_pk_bf16_f32 v4, v118, v119
	v_cvt_pk_bf16_f32 v5, v120, v121
	v_cvt_pk_bf16_f32 v6, v110, v111
	v_cvt_pk_bf16_f32 v7, v112, v113
	s_mov_b32 s33, 0x80000
	v_lshl_add_u64 v[8:9], v[2:3], 0, s[38:39]
	global_store_dwordx4 v[10:11], v[4:7], off
	v_add_co_u32_e32 v10, vcc, s33, v2
	s_nop 0
	v_cvt_pk_bf16_f32 v4, v102, v103
	v_cvt_pk_bf16_f32 v5, v104, v105
	v_cvt_pk_bf16_f32 v6, v98, v99
	v_cvt_pk_bf16_f32 v7, v100, v101
	global_store_dwordx4 v[8:9], v[4:7], off offset:256
	s_mov_b64 s[38:39], 0x80000
	v_addc_co_u32_e32 v11, vcc, 0, v3, vcc
	v_cvt_pk_bf16_f32 v4, v94, v95
	v_cvt_pk_bf16_f32 v5, v96, v97
	v_cvt_pk_bf16_f32 v6, v90, v91
	v_cvt_pk_bf16_f32 v7, v92, v93
	s_mov_b32 s33, 0x90000
	v_lshl_add_u64 v[8:9], v[2:3], 0, s[38:39]
	global_store_dwordx4 v[10:11], v[4:7], off
	v_add_co_u32_e32 v10, vcc, s33, v2
	s_nop 0
	v_cvt_pk_bf16_f32 v4, v82, v83
	v_cvt_pk_bf16_f32 v5, v84, v85
	v_cvt_pk_bf16_f32 v6, v74, v75
	v_cvt_pk_bf16_f32 v7, v76, v77
	global_store_dwordx4 v[8:9], v[4:7], off offset:256
	s_mov_b64 s[38:39], 0x90000
	v_addc_co_u32_e32 v11, vcc, 0, v3, vcc
	v_cvt_pk_bf16_f32 v4, v86, v87
	v_cvt_pk_bf16_f32 v5, v88, v89
	v_cvt_pk_bf16_f32 v6, v78, v79
	v_cvt_pk_bf16_f32 v7, v80, v81
	s_mov_b32 s33, 0xa0000
	v_lshl_add_u64 v[8:9], v[2:3], 0, s[38:39]
	global_store_dwordx4 v[10:11], v[4:7], off
	s_mov_b64 s[38:39], 0xa0000
	v_add_co_u32_e32 v10, vcc, s33, v2
	v_cvt_pk_bf16_f32 v4, v66, v67
	v_cvt_pk_bf16_f32 v5, v68, v69
	v_cvt_pk_bf16_f32 v6, v58, v59
	v_cvt_pk_bf16_f32 v7, v60, v61
	global_store_dwordx4 v[8:9], v[4:7], off offset:256
	v_lshl_add_u64 v[8:9], v[2:3], 0, s[38:39]
	v_addc_co_u32_e32 v11, vcc, 0, v3, vcc
	v_cvt_pk_bf16_f32 v4, v70, v71
	v_cvt_pk_bf16_f32 v5, v72, v73
	v_cvt_pk_bf16_f32 v6, v62, v63
	v_cvt_pk_bf16_f32 v7, v64, v65
	s_mov_b64 s[38:39], 0xb0000
	s_mov_b32 s33, 0xb0000
	global_store_dwordx4 v[10:11], v[4:7], off
	s_mov_b32 s35, s8
	s_mov_b64 s[40:41], s[36:37]
	v_cvt_pk_bf16_f32 v4, v50, v51
	v_cvt_pk_bf16_f32 v5, v52, v53
	v_cvt_pk_bf16_f32 v6, v42, v43
	v_cvt_pk_bf16_f32 v7, v44, v45
	global_store_dwordx4 v[8:9], v[4:7], off offset:256
	v_lshl_add_u64 v[8:9], v[2:3], 0, s[38:39]
	v_add_co_u32_e32 v2, vcc, s33, v2
	v_cvt_pk_bf16_f32 v4, v54, v55
	v_cvt_pk_bf16_f32 v5, v56, v57
	s_mov_b32 s33, s9
	s_nop 0
	v_addc_co_u32_e32 v3, vcc, 0, v3, vcc
	s_and_b64 vcc, exec, s[6:7]
	s_mov_b64 s[38:39], s[28:29]
	v_cvt_pk_bf16_f32 v6, v46, v47
	v_cvt_pk_bf16_f32 v7, v48, v49
	global_store_dwordx4 v[2:3], v[4:7], off
	v_cvt_pk_bf16_f32 v2, v38, v39
	v_cvt_pk_bf16_f32 v3, v40, v41
	s_nop 1
	v_cvt_pk_bf16_f32 v4, v34, v35
	v_cvt_pk_bf16_f32 v5, v36, v37
	global_store_dwordx4 v[8:9], v[2:5], off offset:256
	s_cbranch_vccz .LBB0_698
	s_waitcnt vmcnt(0)
	s_cmpk_gt_u32 s10, 0xff
	s_cbranch_scc1 .LBB0_709
	s_barrier

.LBB0_1192:
	s_xor_b64 s[38:39], s[8:9], -1
	v_readfirstlane_b32 s26, v2
	v_readfirstlane_b32 s27, v3
	s_add_u32 s40, s10, s26
	s_addc_u32 s41, s13, s27
	v_readfirstlane_b32 s36, v4
	s_and_b64 s[42:43], s[8:9], exec
	v_readfirstlane_b32 s37, v5
	s_cselect_b32 s57, s41, s45
	s_cselect_b32 s58, s40, s44
	s_add_u32 s42, s14, s36
	s_addc_u32 s43, s16, s37
	s_and_b64 s[8:9], s[8:9], exec
	s_cselect_b32 s8, s43, s47
	s_cselect_b32 s9, s42, s46
	s_add_u32 s44, s44, 0x30080
	s_addc_u32 s45, s45, 0
	s_add_u32 s59, s46, 0x100
	s_addc_u32 s60, s47, 0
	s_mov_b32 s61, -2
	s_add_u32 s46, s44, 0xfffd0080
	s_addc_u32 s47, s45, -1
	s_add_i32 s63, 0, 0x10000
	v_add_u32_e32 v14, s63, v182
	ds_read_b128 v[2:5], v14
	ds_read_b128 v[6:9], v14 offset:1024
	ds_read_b128 v[10:13], v14 offset:2048
	ds_read_b128 v[14:17], v14 offset:3072
	s_cmp_eq_u32 s61, 8
	s_cselect_b32 s53, s57, s47
	s_cselect_b32 s52, s58, s46
	s_cselect_b32 s47, s8, s60
	s_cselect_b32 s46, s9, s59
	v_lshl_add_u64 v[18:19], s[44:45], 0, v[168:169]
	s_add_i32 m0, s18, 0xc000
	ds_read_b128 v[200:203], v184
	ds_read_b128 v[204:207], v184 offset:1024
	ds_read_b128 v[208:211], v184 offset:2048
	ds_read_b128 v[212:215], v184 offset:3072
	ds_read_b128 v[220:223], v184 offset:4096
	ds_read_b128 v[224:227], v184 offset:5120
	ds_read_b128 v[232:235], v184 offset:6144
	ds_read_b128 v[236:239], v184 offset:7168
	global_load_lds_dwordx4 v[18:19], off
	v_lshl_add_u64 v[18:19], s[44:45], 0, v[170:171]
	s_add_i32 m0, s18, 0xe000
	s_nop 0
	global_load_lds_dwordx4 v[18:19], off
	s_waitcnt lgkmcnt(8)
	s_barrier
	s_waitcnt lgkmcnt(0)
	s_setprio 1
	s_waitcnt lgkmcnt(0)
	v_mfma_scale_f32_16x16x128_f8f6f4 v[158:161], v[2:9], v[200:207], 0, v1, v180 op_sel_hi:[0,0,0]
	v_mfma_scale_f32_16x16x128_f8f6f4 v[154:157], v[10:17], v[200:207], 0, v1, v180 op_sel_hi:[0,0,0]
	v_mfma_scale_f32_16x16x128_f8f6f4 v[150:153], v[2:9], v[208:215], 0, v1, v180 op_sel_hi:[0,0,0]
	v_mfma_scale_f32_16x16x128_f8f6f4 v[142:145], v[10:17], v[208:215], 0, v1, v180 op_sel_hi:[0,0,0]
	v_mfma_scale_f32_16x16x128_f8f6f4 v[134:137], v[2:9], v[220:227], 0, v1, v180 op_sel_hi:[0,0,0]
	v_mfma_scale_f32_16x16x128_f8f6f4 v[126:129], v[10:17], v[220:227], 0, v1, v180 op_sel_hi:[0,0,0]
	v_mfma_scale_f32_16x16x128_f8f6f4 v[118:121], v[2:9], v[232:239], 0, v1, v180 op_sel_hi:[0,0,0]
	v_mfma_scale_f32_16x16x128_f8f6f4 v[110:113], v[10:17], v[232:239], 0, v1, v180 op_sel_hi:[0,0,0]
	s_setprio 0
	s_barrier
	s_add_i32 s62, 0, 0x14000
	s_add_i32 s63, s63, s17
	v_add_u32_e32 v30, s62, v182
	v_lshl_add_u64 v[172:173], s[46:47], 0, v[194:195]
	s_mov_b32 m0, s63
	ds_read_b128 v[18:21], v30
	ds_read_b128 v[22:25], v30 offset:1024
	ds_read_b128 v[26:29], v30 offset:2048
	ds_read_b128 v[30:33], v30 offset:3072
	global_load_lds_dwordx4 v[172:173], off
	v_lshl_add_u64 v[174:175], s[46:47], 0, v[166:167]
	s_add_i32 m0, s63, 0x2000
	s_nop 0
	global_load_lds_dwordx4 v[174:175], off
	s_barrier
	s_waitcnt lgkmcnt(0)
	s_setprio 1
	s_waitcnt lgkmcnt(0)
	v_mfma_scale_f32_16x16x128_f8f6f4 v[146:149], v[18:25], v[200:207], 0, v1, v180 op_sel_hi:[0,0,0]
	v_mfma_scale_f32_16x16x128_f8f6f4 v[138:141], v[26:33], v[200:207], 0, v1, v180 op_sel_hi:[0,0,0]
	v_mfma_scale_f32_16x16x128_f8f6f4 v[130:133], v[18:25], v[208:215], 0, v1, v180 op_sel_hi:[0,0,0]
	v_mfma_scale_f32_16x16x128_f8f6f4 v[122:125], v[26:33], v[208:215], 0, v1, v180 op_sel_hi:[0,0,0]
	v_mfma_scale_f32_16x16x128_f8f6f4 v[114:117], v[18:25], v[220:227], 0, v1, v180 op_sel_hi:[0,0,0]
	v_mfma_scale_f32_16x16x128_f8f6f4 v[106:109], v[26:33], v[220:227], 0, v1, v180 op_sel_hi:[0,0,0]
	v_mfma_scale_f32_16x16x128_f8f6f4 v[102:105], v[18:25], v[232:239], 0, v1, v180 op_sel_hi:[0,0,0]
	v_mfma_scale_f32_16x16x128_f8f6f4 v[98:101], v[26:33], v[232:239], 0, v1, v180 op_sel_hi:[0,0,0]
	s_setprio 0
	s_mov_b32 m0, s18
	v_lshl_add_u64 v[176:177], s[52:53], 0, v[162:163]
	s_barrier
	ds_read_b128 v[200:203], v184 offset:16384
	ds_read_b128 v[204:207], v184 offset:17408
	ds_read_b128 v[208:211], v184 offset:18432
	ds_read_b128 v[212:215], v184 offset:19456
	ds_read_b128 v[220:223], v184 offset:20480
	ds_read_b128 v[224:227], v184 offset:21504
	ds_read_b128 v[232:235], v184 offset:22528
	ds_read_b128 v[236:239], v184 offset:23552
	global_load_lds_dwordx4 v[176:177], off
	v_lshl_add_u64 v[178:179], s[52:53], 0, v[164:165]
	s_mov_b32 m0, s19
	s_nop 0
	global_load_lds_dwordx4 v[178:179], off
	s_barrier
	s_waitcnt lgkmcnt(0)
	s_setprio 1
	s_waitcnt lgkmcnt(0)
	v_mfma_scale_f32_16x16x128_f8f6f4 v[94:97], v[2:9], v[200:207], 0, v1, v180 op_sel_hi:[0,0,0]
	v_mfma_scale_f32_16x16x128_f8f6f4 v[90:93], v[10:17], v[200:207], 0, v1, v180 op_sel_hi:[0,0,0]
	v_mfma_scale_f32_16x16x128_f8f6f4 v[86:89], v[2:9], v[208:215], 0, v1, v180 op_sel_hi:[0,0,0]
	v_mfma_scale_f32_16x16x128_f8f6f4 v[78:81], v[10:17], v[208:215], 0, v1, v180 op_sel_hi:[0,0,0]
	v_mfma_scale_f32_16x16x128_f8f6f4 v[70:73], v[2:9], v[220:227], 0, v1, v180 op_sel_hi:[0,0,0]
	v_mfma_scale_f32_16x16x128_f8f6f4 v[62:65], v[10:17], v[220:227], 0, v1, v180 op_sel_hi:[0,0,0]
	v_mfma_scale_f32_16x16x128_f8f6f4 v[54:57], v[2:9], v[232:239], 0, v1, v180 op_sel_hi:[0,0,0]
	v_mfma_scale_f32_16x16x128_f8f6f4 v[46:49], v[10:17], v[232:239], 0, v1, v180 op_sel_hi:[0,0,0]
	s_setprio 0
	s_barrier
	s_add_u32 s64, s46, 0x30000
	s_addc_u32 s65, s47, 0
	s_add_i32 s62, s62, s17
	v_lshl_add_u64 v[2:3], s[64:65], 0, v[194:195]
	s_mov_b32 m0, s62
	s_nop 0
	global_load_lds_dwordx4 v[2:3], off
	v_lshl_add_u64 v[2:3], s[64:65], 0, v[166:167]
	s_add_i32 m0, s62, 0x2000
	s_nop 0
	global_load_lds_dwordx4 v[2:3], off
	s_waitcnt vmcnt(6)
	s_barrier
	s_setprio 1
	v_mfma_scale_f32_16x16x128_f8f6f4 v[82:85], v[18:25], v[200:207], 0, v1, v180 op_sel_hi:[0,0,0]
	v_mfma_scale_f32_16x16x128_f8f6f4 v[74:77], v[26:33], v[200:207], 0, v1, v180 op_sel_hi:[0,0,0]
	v_mfma_scale_f32_16x16x128_f8f6f4 v[66:69], v[18:25], v[208:215], 0, v1, v180 op_sel_hi:[0,0,0]
	v_mfma_scale_f32_16x16x128_f8f6f4 v[58:61], v[26:33], v[208:215], 0, v1, v180 op_sel_hi:[0,0,0]
	v_mfma_scale_f32_16x16x128_f8f6f4 v[50:53], v[18:25], v[220:227], 0, v1, v180 op_sel_hi:[0,0,0]
	v_mfma_scale_f32_16x16x128_f8f6f4 v[42:45], v[26:33], v[220:227], 0, v1, v180 op_sel_hi:[0,0,0]
	v_mfma_scale_f32_16x16x128_f8f6f4 v[38:41], v[18:25], v[232:239], 0, v1, v180 op_sel_hi:[0,0,0]
	v_mfma_scale_f32_16x16x128_f8f6f4 v[34:37], v[26:33], v[232:239], 0, v1, v180 op_sel_hi:[0,0,0]
	s_setprio 0
	s_add_i32 s62, 0, 0x18000
	v_add_u32_e32 v14, s62, v182
	s_barrier
	ds_read_b128 v[2:5], v14
	ds_read_b128 v[6:9], v14 offset:1024
	ds_read_b128 v[10:13], v14 offset:2048
	ds_read_b128 v[14:17], v14 offset:3072
	s_add_u32 s52, s52, 0x30000
	s_addc_u32 s53, s53, 0
	s_mov_b32 m0, s24
	v_lshl_add_u64 v[188:189], s[52:53], 0, v[162:163]
	ds_read_b128 v[18:21], v184 offset:32768
	ds_read_b128 v[22:25], v184 offset:33792
	ds_read_b128 v[26:29], v184 offset:34816
	ds_read_b128 v[30:33], v184 offset:35840
	ds_read_b128 v[200:203], v184 offset:36864
	ds_read_b128 v[204:207], v184 offset:37888
	ds_read_b128 v[208:211], v184 offset:38912
	ds_read_b128 v[212:215], v184 offset:39936
	global_load_lds_dwordx4 v[188:189], off
	v_lshl_add_u64 v[188:189], s[52:53], 0, v[164:165]
	s_mov_b32 m0, s25
	s_nop 0
	global_load_lds_dwordx4 v[188:189], off
	s_waitcnt lgkmcnt(8)
	s_barrier
	s_waitcnt lgkmcnt(0)
	s_setprio 1
	s_waitcnt lgkmcnt(0)
	v_mfma_scale_f32_16x16x128_f8f6f4 v[158:161], v[2:9], v[18:25], v[158:161], v1, v180 op_sel_hi:[0,0,0]
	v_mfma_scale_f32_16x16x128_f8f6f4 v[154:157], v[10:17], v[18:25], v[154:157], v1, v180 op_sel_hi:[0,0,0]
	v_mfma_scale_f32_16x16x128_f8f6f4 v[150:153], v[2:9], v[26:33], v[150:153], v1, v180 op_sel_hi:[0,0,0]
	v_mfma_scale_f32_16x16x128_f8f6f4 v[142:145], v[10:17], v[26:33], v[142:145], v1, v180 op_sel_hi:[0,0,0]
	v_mfma_scale_f32_16x16x128_f8f6f4 v[134:137], v[2:9], v[200:207], v[134:137], v1, v180 op_sel_hi:[0,0,0]
	v_mfma_scale_f32_16x16x128_f8f6f4 v[126:129], v[10:17], v[200:207], v[126:129], v1, v180 op_sel_hi:[0,0,0]
	v_mfma_scale_f32_16x16x128_f8f6f4 v[118:121], v[2:9], v[208:215], v[118:121], v1, v180 op_sel_hi:[0,0,0]
	v_mfma_scale_f32_16x16x128_f8f6f4 v[110:113], v[10:17], v[208:215], v[110:113], v1, v180 op_sel_hi:[0,0,0]
	s_setprio 0
	s_barrier
	s_add_i32 s52, 0, 0x1c000
	s_add_i32 s53, s62, s17
	v_add_u32_e32 v187, s52, v182
	v_lshl_add_u64 v[172:173], v[172:173], 0, s[30:31]
	s_mov_b32 m0, s53
	ds_read_b128 v[220:223], v187
	ds_read_b128 v[224:227], v187 offset:1024
	ds_read_b128 v[232:235], v187 offset:2048
	ds_read_b128 v[236:239], v187 offset:3072
	global_load_lds_dwordx4 v[172:173], off
	v_lshl_add_u64 v[172:173], v[174:175], 0, s[30:31]
	s_add_i32 m0, s53, 0x2000
	s_nop 0
	global_load_lds_dwordx4 v[172:173], off
	s_barrier
	s_waitcnt lgkmcnt(0)
	s_setprio 1
	s_waitcnt lgkmcnt(0)
	v_mfma_scale_f32_16x16x128_f8f6f4 v[146:149], v[220:227], v[18:25], v[146:149], v1, v180 op_sel_hi:[0,0,0]
	v_mfma_scale_f32_16x16x128_f8f6f4 v[138:141], v[232:239], v[18:25], v[138:141], v1, v180 op_sel_hi:[0,0,0]
	v_mfma_scale_f32_16x16x128_f8f6f4 v[130:133], v[220:227], v[26:33], v[130:133], v1, v180 op_sel_hi:[0,0,0]
	v_mfma_scale_f32_16x16x128_f8f6f4 v[122:125], v[232:239], v[26:33], v[122:125], v1, v180 op_sel_hi:[0,0,0]
	v_mfma_scale_f32_16x16x128_f8f6f4 v[114:117], v[220:227], v[200:207], v[114:117], v1, v180 op_sel_hi:[0,0,0]
	v_mfma_scale_f32_16x16x128_f8f6f4 v[106:109], v[232:239], v[200:207], v[106:109], v1, v180 op_sel_hi:[0,0,0]
	v_mfma_scale_f32_16x16x128_f8f6f4 v[102:105], v[220:227], v[208:215], v[102:105], v1, v180 op_sel_hi:[0,0,0]
	v_mfma_scale_f32_16x16x128_f8f6f4 v[98:101], v[232:239], v[208:215], v[98:101], v1, v180 op_sel_hi:[0,0,0]
	s_setprio 0
	s_mov_b32 m0, s33
	v_lshl_add_u64 v[172:173], v[176:177], 0, s[30:31]
	s_barrier
	ds_read_b128 v[18:21], v184 offset:49152
	ds_read_b128 v[22:25], v184 offset:50176
	ds_read_b128 v[26:29], v184 offset:51200
	ds_read_b128 v[30:33], v184 offset:52224
	ds_read_b128 v[200:203], v184 offset:53248
	ds_read_b128 v[204:207], v184 offset:54272
	ds_read_b128 v[208:211], v184 offset:55296
	ds_read_b128 v[212:215], v184 offset:56320
	global_load_lds_dwordx4 v[172:173], off
	v_lshl_add_u64 v[172:173], v[178:179], 0, s[30:31]
	s_mov_b32 m0, s35
	s_nop 0
	global_load_lds_dwordx4 v[172:173], off
	s_barrier
	s_waitcnt lgkmcnt(0)
	s_setprio 1
	s_waitcnt lgkmcnt(0)
	v_mfma_scale_f32_16x16x128_f8f6f4 v[94:97], v[2:9], v[18:25], v[94:97], v1, v180 op_sel_hi:[0,0,0]
	v_mfma_scale_f32_16x16x128_f8f6f4 v[90:93], v[10:17], v[18:25], v[90:93], v1, v180 op_sel_hi:[0,0,0]
	v_mfma_scale_f32_16x16x128_f8f6f4 v[86:89], v[2:9], v[26:33], v[86:89], v1, v180 op_sel_hi:[0,0,0]
	v_mfma_scale_f32_16x16x128_f8f6f4 v[78:81], v[10:17], v[26:33], v[78:81], v1, v180 op_sel_hi:[0,0,0]
	v_mfma_scale_f32_16x16x128_f8f6f4 v[70:73], v[2:9], v[200:207], v[70:73], v1, v180 op_sel_hi:[0,0,0]
	v_mfma_scale_f32_16x16x128_f8f6f4 v[62:65], v[10:17], v[200:207], v[62:65], v1, v180 op_sel_hi:[0,0,0]
	v_mfma_scale_f32_16x16x128_f8f6f4 v[54:57], v[2:9], v[208:215], v[54:57], v1, v180 op_sel_hi:[0,0,0]
	v_mfma_scale_f32_16x16x128_f8f6f4 v[46:49], v[10:17], v[208:215], v[46:49], v1, v180 op_sel_hi:[0,0,0]
	s_setprio 0
	s_barrier
	s_add_u32 s46, s46, 0x30080
	s_addc_u32 s47, s47, 0
	s_add_i32 s52, s52, s17
	v_lshl_add_u64 v[2:3], s[46:47], 0, v[194:195]
	s_mov_b32 m0, s52
	s_nop 0
	global_load_lds_dwordx4 v[2:3], off
	v_lshl_add_u64 v[2:3], s[46:47], 0, v[166:167]
	s_add_i32 m0, s52, 0x2000
	s_nop 0
	global_load_lds_dwordx4 v[2:3], off
	s_waitcnt vmcnt(6)
	s_barrier
	s_setprio 1
	v_mfma_scale_f32_16x16x128_f8f6f4 v[82:85], v[220:227], v[18:25], v[82:85], v1, v180 op_sel_hi:[0,0,0]
	v_mfma_scale_f32_16x16x128_f8f6f4 v[74:77], v[232:239], v[18:25], v[74:77], v1, v180 op_sel_hi:[0,0,0]
	v_mfma_scale_f32_16x16x128_f8f6f4 v[66:69], v[220:227], v[26:33], v[66:69], v1, v180 op_sel_hi:[0,0,0]
	v_mfma_scale_f32_16x16x128_f8f6f4 v[58:61], v[232:239], v[26:33], v[58:61], v1, v180 op_sel_hi:[0,0,0]
	v_mfma_scale_f32_16x16x128_f8f6f4 v[50:53], v[220:227], v[200:207], v[50:53], v1, v180 op_sel_hi:[0,0,0]
	v_mfma_scale_f32_16x16x128_f8f6f4 v[42:45], v[232:239], v[200:207], v[42:45], v1, v180 op_sel_hi:[0,0,0]
	v_mfma_scale_f32_16x16x128_f8f6f4 v[38:41], v[220:227], v[208:215], v[38:41], v1, v180 op_sel_hi:[0,0,0]
	v_mfma_scale_f32_16x16x128_f8f6f4 v[34:37], v[232:239], v[208:215], v[34:37], v1, v180 op_sel_hi:[0,0,0]
	s_setprio 0
	s_add_i32 s61, s61, 2
	s_add_u32 s44, s44, 0x100
	s_addc_u32 s45, s45, 0
	s_add_u32 s59, s59, 0x100
	s_addc_u32 s60, s60, 0
	s_cmp_gt_u32 s61, 9
	s_barrier
	s_cbranch_scc1 .Lpk1193_exit

.Lpk1193_exit:
	v_add_u32_e32 v2, s56, v181
	v_ashrrev_i32_e32 v3, 31, v2
	v_add_u32_e32 v4, s55, v183
	v_lshlrev_b64 v[2:3], 12, v[2:3]
	v_ashrrev_i32_e32 v5, 31, v4
	v_lshl_add_u64 v[2:3], s[6:7], 0, v[2:3]
	v_lshl_add_u64 v[2:3], v[4:5], 1, v[2:3]
	s_mov_b64 s[8:9], 0x10000
	s_nop 15
	s_nop 15
	v_cvt_pk_bf16_f32 v4, v158, v159
	v_cvt_pk_bf16_f32 v5, v160, v161
	v_cvt_pk_bf16_f32 v6, v154, v155
	v_cvt_pk_bf16_f32 v7, v156, v157
	v_lshl_add_u64 v[8:9], v[2:3], 0, s[8:9]
	s_mov_b32 s8, 0x10000
	global_store_dwordx4 v[2:3], v[4:7], off
	v_add_co_u32_e32 v10, vcc, s8, v2
	s_nop 0
	v_cvt_pk_bf16_f32 v4, v146, v147
	v_cvt_pk_bf16_f32 v5, v148, v149
	v_cvt_pk_bf16_f32 v6, v138, v139
	v_cvt_pk_bf16_f32 v7, v140, v141
	global_store_dwordx4 v[2:3], v[4:7], off offset:256
	v_addc_co_u32_e32 v11, vcc, 0, v3, vcc
	s_nop 0
	v_cvt_pk_bf16_f32 v4, v150, v151
	v_cvt_pk_bf16_f32 v5, v152, v153
	v_cvt_pk_bf16_f32 v6, v142, v143
	v_cvt_pk_bf16_f32 v7, v144, v145
	s_mov_b64 s[8:9], 0x20000
	global_store_dwordx4 v[10:11], v[4:7], off
	v_readfirstlane_b32 s53, v185
	v_readfirstlane_b32 s52, v186
	v_cvt_pk_bf16_f32 v4, v130, v131
	v_cvt_pk_bf16_f32 v5, v132, v133
	v_cvt_pk_bf16_f32 v6, v122, v123
	v_cvt_pk_bf16_f32 v7, v124, v125
	global_store_dwordx4 v[8:9], v[4:7], off offset:256
	v_lshl_add_u64 v[8:9], v[2:3], 0, s[8:9]
	s_mov_b32 s8, 0x20000
	v_add_co_u32_e32 v10, vcc, s8, v2
	v_cvt_pk_bf16_f32 v4, v134, v135
	v_cvt_pk_bf16_f32 v5, v136, v137
	v_cvt_pk_bf16_f32 v6, v126, v127
	v_cvt_pk_bf16_f32 v7, v128, v129
	s_nop 1
	v_addc_co_u32_e32 v11, vcc, 0, v3, vcc
	s_mov_b64 s[8:9], 0x30000
	global_store_dwordx4 v[10:11], v[4:7], off
	s_mov_b32 s55, s52
	s_mov_b32 s56, s53
	v_cvt_pk_bf16_f32 v4, v114, v115
	v_cvt_pk_bf16_f32 v5, v116, v117
	v_cvt_pk_bf16_f32 v6, v106, v107
	v_cvt_pk_bf16_f32 v7, v108, v109
	global_store_dwordx4 v[8:9], v[4:7], off offset:256
	v_lshl_add_u64 v[8:9], v[2:3], 0, s[8:9]
	s_mov_b32 s8, 0x30000
	v_add_co_u32_e32 v10, vcc, s8, v2
	v_cvt_pk_bf16_f32 v4, v118, v119
	v_cvt_pk_bf16_f32 v5, v120, v121
	v_cvt_pk_bf16_f32 v6, v110, v111
	v_cvt_pk_bf16_f32 v7, v112, v113
	s_nop 1
	v_addc_co_u32_e32 v11, vcc, 0, v3, vcc
	s_mov_b64 s[8:9], 0x80000
	global_store_dwordx4 v[10:11], v[4:7], off
	s_mov_b64 s[46:47], s[42:43]
	s_mov_b64 s[44:45], s[40:41]
	v_cvt_pk_bf16_f32 v4, v102, v103
	v_cvt_pk_bf16_f32 v5, v104, v105
	v_cvt_pk_bf16_f32 v6, v98, v99
	v_cvt_pk_bf16_f32 v7, v100, v101
	global_store_dwordx4 v[8:9], v[4:7], off offset:256
	v_lshl_add_u64 v[8:9], v[2:3], 0, s[8:9]
	s_mov_b32 s8, 0x80000
	v_add_co_u32_e32 v10, vcc, s8, v2
	v_cvt_pk_bf16_f32 v4, v94, v95
	v_cvt_pk_bf16_f32 v5, v96, v97
	v_cvt_pk_bf16_f32 v6, v90, v91
	v_cvt_pk_bf16_f32 v7, v92, v93
	s_nop 1
	v_addc_co_u32_e32 v11, vcc, 0, v3, vcc
	s_mov_b64 s[8:9], 0x90000
	global_store_dwordx4 v[10:11], v[4:7], off
	s_nop 1
	v_cvt_pk_bf16_f32 v4, v82, v83
	v_cvt_pk_bf16_f32 v5, v84, v85
	v_cvt_pk_bf16_f32 v6, v74, v75
	v_cvt_pk_bf16_f32 v7, v76, v77
	global_store_dwordx4 v[8:9], v[4:7], off offset:256
	v_lshl_add_u64 v[8:9], v[2:3], 0, s[8:9]
	s_mov_b32 s8, 0x90000
	v_add_co_u32_e32 v10, vcc, s8, v2
	v_cvt_pk_bf16_f32 v4, v86, v87
	v_cvt_pk_bf16_f32 v5, v88, v89
	v_cvt_pk_bf16_f32 v6, v78, v79
	v_cvt_pk_bf16_f32 v7, v80, v81
	s_nop 1
	v_addc_co_u32_e32 v11, vcc, 0, v3, vcc
	s_mov_b64 s[8:9], 0xa0000
	global_store_dwordx4 v[10:11], v[4:7], off
	s_nop 1
	v_cvt_pk_bf16_f32 v4, v66, v67
	v_cvt_pk_bf16_f32 v5, v68, v69
	v_cvt_pk_bf16_f32 v6, v58, v59
	v_cvt_pk_bf16_f32 v7, v60, v61
	global_store_dwordx4 v[8:9], v[4:7], off offset:256
	v_lshl_add_u64 v[8:9], v[2:3], 0, s[8:9]
	s_mov_b32 s8, 0xa0000
	v_add_co_u32_e32 v10, vcc, s8, v2
	v_cvt_pk_bf16_f32 v4, v70, v71
	v_cvt_pk_bf16_f32 v5, v72, v73
	v_cvt_pk_bf16_f32 v6, v62, v63
	v_cvt_pk_bf16_f32 v7, v64, v65
	s_nop 1
	v_addc_co_u32_e32 v11, vcc, 0, v3, vcc
	s_mov_b64 s[8:9], 0xb0000
	global_store_dwordx4 v[10:11], v[4:7], off
	s_nop 1
	v_cvt_pk_bf16_f32 v4, v50, v51
	v_cvt_pk_bf16_f32 v5, v52, v53
	v_cvt_pk_bf16_f32 v6, v42, v43
	v_cvt_pk_bf16_f32 v7, v44, v45
	global_store_dwordx4 v[8:9], v[4:7], off offset:256
	v_lshl_add_u64 v[8:9], v[2:3], 0, s[8:9]
	s_mov_b32 s8, 0xb0000
	v_add_co_u32_e32 v2, vcc, s8, v2
	v_cvt_pk_bf16_f32 v4, v54, v55
	v_cvt_pk_bf16_f32 v5, v56, v57
	v_cvt_pk_bf16_f32 v6, v46, v47
	v_cvt_pk_bf16_f32 v7, v48, v49
	s_nop 1
	v_addc_co_u32_e32 v3, vcc, 0, v3, vcc
	s_and_b64 vcc, exec, s[38:39]
	global_store_dwordx4 v[2:3], v[4:7], off
	v_cvt_pk_bf16_f32 v2, v38, v39
	v_cvt_pk_bf16_f32 v3, v40, v41
	s_nop 1
	v_cvt_pk_bf16_f32 v4, v34, v35
	v_cvt_pk_bf16_f32 v5, v36, v37
	global_store_dwordx4 v[8:9], v[2:5], off offset:256
	s_cbranch_vccz .LBB0_1187
	s_branch .LBB0_1196
